# one-operand-per-step MFMA path with group starts chosen from the previous group's last operand blocks
# speedup vs baseline: 1.0025x; 1.0011x over previous
.LBB0_318:
	ds_read_b128 v[26:29], v185
	ds_read_b128 v[30:33], v185 offset:1024
	ds_read_b128 v[18:21], v185 offset:2048
	ds_read_b128 v[22:25], v185 offset:3072
	ds_read_b128 v[10:13], v186
	ds_read_b128 v[14:17], v186 offset:1024
	ds_read_b128 v[2:5], v186 offset:2048
	ds_read_b128 v[6:9], v186 offset:3072
	s_add_u32 s24, s26, 0xffea8080
	s_addc_u32 s25, s27, -1
	s_cmpk_eq_i32 s58, 0x52
	s_cselect_b32 s31, s5, s25
	s_cselect_b32 s30, s4, s24
	s_cselect_b32 s29, s21, s51
	s_cselect_b32 s28, s20, s50
	v_lshl_add_u64 v[212:213], s[26:27], 0, v[166:167]
	s_add_i32 m0, s7, 0xc000
	ds_read_b128 v[174:177], v187
	ds_read_b128 v[178:181], v187 offset:1024
	ds_read_b128 v[188:191], v187 offset:2048
	ds_read_b128 v[192:195], v187 offset:3072
	ds_read_b128 v[196:199], v187 offset:4096
	ds_read_b128 v[200:203], v187 offset:5120
	ds_read_b128 v[204:207], v187 offset:6144
	ds_read_b128 v[208:211], v187 offset:7168
	global_load_lds_dwordx4 v[212:213], off
	v_lshl_add_u64 v[212:213], s[26:27], 0, v[168:169]
	s_add_i32 m0, s7, 0xe000
	s_nop 0
	global_load_lds_dwordx4 v[212:213], off
	s_waitcnt vmcnt(8)
	s_waitcnt lgkmcnt(0)
	s_barrier
	s_setprio 1
	s_waitcnt lgkmcnt(0)
	v_mfma_scale_f32_16x16x128_f8f6f4 v[158:161], v[26:33], v[174:181], v[158:161], v1, v1 op_sel_hi:[0,0,0]
	v_mfma_scale_f32_16x16x128_f8f6f4 v[154:157], v[18:25], v[174:181], v[154:157], v1, v1 op_sel_hi:[0,0,0]
	v_mfma_scale_f32_16x16x128_f8f6f4 v[138:141], v[18:25], v[188:195], v[138:141], v1, v1 op_sel_hi:[0,0,0]
	v_mfma_scale_f32_16x16x128_f8f6f4 v[142:145], v[26:33], v[188:195], v[142:145], v1, v1 op_sel_hi:[0,0,0]
	v_mfma_scale_f32_16x16x128_f8f6f4 v[126:129], v[26:33], v[196:203], v[126:129], v1, v1 op_sel_hi:[0,0,0]
	v_mfma_scale_f32_16x16x128_f8f6f4 v[122:125], v[18:25], v[196:203], v[122:125], v1, v1 op_sel_hi:[0,0,0]
	v_mfma_scale_f32_16x16x128_f8f6f4 v[106:109], v[18:25], v[204:211], v[106:109], v1, v1 op_sel_hi:[0,0,0]
	v_mfma_scale_f32_16x16x128_f8f6f4 v[110:113], v[26:33], v[204:211], v[110:113], v1, v1 op_sel_hi:[0,0,0]
	s_setprio 0
	s_setprio 1
	v_mfma_scale_f32_16x16x128_f8f6f4 v[102:105], v[10:17], v[204:211], v[102:105], v1, v1 op_sel_hi:[0,0,0]
	v_mfma_scale_f32_16x16x128_f8f6f4 v[98:101], v[2:9], v[204:211], v[98:101], v1, v1 op_sel_hi:[0,0,0]
	v_mfma_scale_f32_16x16x128_f8f6f4 v[146:149], v[2:9], v[174:181], v[146:149], v1, v1 op_sel_hi:[0,0,0]
	v_mfma_scale_f32_16x16x128_f8f6f4 v[150:153], v[10:17], v[174:181], v[150:153], v1, v1 op_sel_hi:[0,0,0]
	v_mfma_scale_f32_16x16x128_f8f6f4 v[134:137], v[10:17], v[188:195], v[134:137], v1, v1 op_sel_hi:[0,0,0]
	v_mfma_scale_f32_16x16x128_f8f6f4 v[130:133], v[2:9], v[188:195], v[130:133], v1, v1 op_sel_hi:[0,0,0]
	v_mfma_scale_f32_16x16x128_f8f6f4 v[114:117], v[2:9], v[196:203], v[114:117], v1, v1 op_sel_hi:[0,0,0]
	v_mfma_scale_f32_16x16x128_f8f6f4 v[118:121], v[10:17], v[196:203], v[118:121], v1, v1 op_sel_hi:[0,0,0]
	s_setprio 0
	s_barrier
	s_add_i32 s24, s42, s3
	v_lshl_add_u64 v[174:175], s[28:29], 0, v[164:165]
	s_mov_b32 m0, s24
	ds_read_b128 v[188:191], v187 offset:16384
	ds_read_b128 v[192:195], v187 offset:17408
	ds_read_b128 v[196:199], v187 offset:18432
	ds_read_b128 v[200:203], v187 offset:19456
	ds_read_b128 v[204:207], v187 offset:20480
	ds_read_b128 v[208:211], v187 offset:21504
	ds_read_b128 v[212:215], v187 offset:22528
	ds_read_b128 v[216:219], v187 offset:23552
	global_load_lds_dwordx4 v[174:175], off
	s_add_i32 m0, s24, 0x2000
	s_add_u32 s24, s28, 0x158000
	v_lshl_add_u64 v[176:177], s[28:29], 0, v[162:163]
	s_addc_u32 s25, s29, 0
	s_add_i32 s59, s43, s3
	global_load_lds_dwordx4 v[176:177], off
	v_lshl_add_u64 v[178:179], s[24:25], 0, v[164:165]
	s_mov_b32 m0, s59
	v_lshl_add_u64 v[180:181], s[30:31], 0, v[162:163]
	global_load_lds_dwordx4 v[178:179], off
	v_lshl_add_u64 v[178:179], s[24:25], 0, v[162:163]
	s_add_i32 m0, s59, 0x2000
	s_nop 0
	global_load_lds_dwordx4 v[178:179], off
	v_lshl_add_u64 v[178:179], s[30:31], 0, v[164:165]
	s_mov_b32 m0, s7
	s_nop 0
	global_load_lds_dwordx4 v[178:179], off
	s_mov_b32 m0, s17
	s_nop 0
	global_load_lds_dwordx4 v[180:181], off
	s_waitcnt vmcnt(8)
	s_waitcnt lgkmcnt(0)
	s_barrier
	s_setprio 1
	s_waitcnt lgkmcnt(0)
	v_mfma_scale_f32_16x16x128_f8f6f4 v[78:81], v[26:33], v[196:203], v[78:81], v1, v1 op_sel_hi:[0,0,0]
	v_mfma_scale_f32_16x16x128_f8f6f4 v[74:77], v[18:25], v[196:203], v[74:77], v1, v1 op_sel_hi:[0,0,0]
	v_mfma_scale_f32_16x16x128_f8f6f4 v[90:93], v[18:25], v[188:195], v[90:93], v1, v1 op_sel_hi:[0,0,0]
	v_mfma_scale_f32_16x16x128_f8f6f4 v[94:97], v[26:33], v[188:195], v[94:97], v1, v1 op_sel_hi:[0,0,0]
	v_mfma_scale_f32_16x16x128_f8f6f4 v[62:65], v[26:33], v[204:211], v[62:65], v1, v1 op_sel_hi:[0,0,0]
	v_mfma_scale_f32_16x16x128_f8f6f4 v[58:61], v[18:25], v[204:211], v[58:61], v1, v1 op_sel_hi:[0,0,0]
	v_mfma_scale_f32_16x16x128_f8f6f4 v[42:45], v[18:25], v[212:219], v[42:45], v1, v1 op_sel_hi:[0,0,0]
	v_mfma_scale_f32_16x16x128_f8f6f4 v[46:49], v[26:33], v[212:219], v[46:49], v1, v1 op_sel_hi:[0,0,0]
	s_setprio 0
	s_setprio 1
	v_mfma_scale_f32_16x16x128_f8f6f4 v[38:41], v[10:17], v[212:219], v[38:41], v1, v1 op_sel_hi:[0,0,0]
	v_mfma_scale_f32_16x16x128_f8f6f4 v[34:37], v[2:9], v[212:219], v[34:37], v1, v1 op_sel_hi:[0,0,0]
	v_mfma_scale_f32_16x16x128_f8f6f4 v[82:85], v[2:9], v[188:195], v[82:85], v1, v1 op_sel_hi:[0,0,0]
	v_mfma_scale_f32_16x16x128_f8f6f4 v[86:89], v[10:17], v[188:195], v[86:89], v1, v1 op_sel_hi:[0,0,0]
	v_mfma_scale_f32_16x16x128_f8f6f4 v[70:73], v[10:17], v[196:203], v[70:73], v1, v1 op_sel_hi:[0,0,0]
	v_mfma_scale_f32_16x16x128_f8f6f4 v[66:69], v[2:9], v[196:203], v[66:69], v1, v1 op_sel_hi:[0,0,0]
	v_mfma_scale_f32_16x16x128_f8f6f4 v[50:53], v[2:9], v[204:211], v[50:53], v1, v1 op_sel_hi:[0,0,0]
	v_mfma_scale_f32_16x16x128_f8f6f4 v[54:57], v[10:17], v[204:211], v[54:57], v1, v1 op_sel_hi:[0,0,0]
	s_setprio 0
	s_barrier
	s_add_i32 s59, 0, 0x18000
	s_add_i32 s60, 0, 0x1c000
	v_add_u32_e32 v14, s59, v183
	v_add_u32_e32 v30, s60, v183
	ds_read_b128 v[2:5], v14
	ds_read_b128 v[6:9], v14 offset:1024
	ds_read_b128 v[10:13], v14 offset:2048
	ds_read_b128 v[14:17], v14 offset:3072
	ds_read_b128 v[18:21], v30
	ds_read_b128 v[22:25], v30 offset:1024
	ds_read_b128 v[26:29], v30 offset:2048
	ds_read_b128 v[30:33], v30 offset:3072
	s_add_u32 s24, s30, 0x158000
	s_addc_u32 s25, s31, 0
	s_mov_b32 m0, s34
	v_lshl_add_u64 v[220:221], s[24:25], 0, v[164:165]
	ds_read_b128 v[188:191], v187 offset:32768
	ds_read_b128 v[192:195], v187 offset:33792
	ds_read_b128 v[196:199], v187 offset:34816
	ds_read_b128 v[200:203], v187 offset:35840
	ds_read_b128 v[204:207], v187 offset:36864
	ds_read_b128 v[208:211], v187 offset:37888
	ds_read_b128 v[212:215], v187 offset:38912
	ds_read_b128 v[216:219], v187 offset:39936
	global_load_lds_dwordx4 v[220:221], off
	v_lshl_add_u64 v[220:221], s[24:25], 0, v[162:163]
	s_mov_b32 m0, s35
	s_nop 0
	global_load_lds_dwordx4 v[220:221], off
	s_waitcnt vmcnt(8)
	s_waitcnt lgkmcnt(0)
	s_barrier
	s_setprio 1
	s_waitcnt lgkmcnt(0)
	v_mfma_scale_f32_16x16x128_f8f6f4 v[122:125], v[10:17], v[204:211], v[122:125], v1, v1 op_sel_hi:[0,0,0]
	v_mfma_scale_f32_16x16x128_f8f6f4 v[126:129], v[2:9], v[204:211], v[126:129], v1, v1 op_sel_hi:[0,0,0]
	v_mfma_scale_f32_16x16x128_f8f6f4 v[158:161], v[2:9], v[188:195], v[158:161], v1, v1 op_sel_hi:[0,0,0]
	v_mfma_scale_f32_16x16x128_f8f6f4 v[154:157], v[10:17], v[188:195], v[154:157], v1, v1 op_sel_hi:[0,0,0]
	v_mfma_scale_f32_16x16x128_f8f6f4 v[138:141], v[10:17], v[196:203], v[138:141], v1, v1 op_sel_hi:[0,0,0]
	v_mfma_scale_f32_16x16x128_f8f6f4 v[142:145], v[2:9], v[196:203], v[142:145], v1, v1 op_sel_hi:[0,0,0]
	v_mfma_scale_f32_16x16x128_f8f6f4 v[110:113], v[2:9], v[212:219], v[110:113], v1, v1 op_sel_hi:[0,0,0]
	v_mfma_scale_f32_16x16x128_f8f6f4 v[106:109], v[10:17], v[212:219], v[106:109], v1, v1 op_sel_hi:[0,0,0]
	s_setprio 0
	s_setprio 1
	v_mfma_scale_f32_16x16x128_f8f6f4 v[102:105], v[18:25], v[212:219], v[102:105], v1, v1 op_sel_hi:[0,0,0]
	v_mfma_scale_f32_16x16x128_f8f6f4 v[98:101], v[26:33], v[212:219], v[98:101], v1, v1 op_sel_hi:[0,0,0]
	v_mfma_scale_f32_16x16x128_f8f6f4 v[146:149], v[26:33], v[188:195], v[146:149], v1, v1 op_sel_hi:[0,0,0]
	v_mfma_scale_f32_16x16x128_f8f6f4 v[150:153], v[18:25], v[188:195], v[150:153], v1, v1 op_sel_hi:[0,0,0]
	v_mfma_scale_f32_16x16x128_f8f6f4 v[134:137], v[18:25], v[196:203], v[134:137], v1, v1 op_sel_hi:[0,0,0]
	v_mfma_scale_f32_16x16x128_f8f6f4 v[130:133], v[26:33], v[196:203], v[130:133], v1, v1 op_sel_hi:[0,0,0]
	v_mfma_scale_f32_16x16x128_f8f6f4 v[114:117], v[26:33], v[204:211], v[114:117], v1, v1 op_sel_hi:[0,0,0]
	v_mfma_scale_f32_16x16x128_f8f6f4 v[118:121], v[18:25], v[204:211], v[118:121], v1, v1 op_sel_hi:[0,0,0]
	s_setprio 0
	s_barrier
	s_add_i32 s24, s59, s3
	v_lshl_add_u64 v[174:175], v[174:175], 0, s[12:13]
	s_mov_b32 m0, s24
	ds_read_b128 v[188:191], v187 offset:49152
	ds_read_b128 v[192:195], v187 offset:50176
	ds_read_b128 v[196:199], v187 offset:51200
	ds_read_b128 v[200:203], v187 offset:52224
	ds_read_b128 v[204:207], v187 offset:53248
	ds_read_b128 v[208:211], v187 offset:54272
	ds_read_b128 v[212:215], v187 offset:55296
	ds_read_b128 v[216:219], v187 offset:56320
	global_load_lds_dwordx4 v[174:175], off
	s_add_i32 m0, s24, 0x2000
	s_add_u32 s24, s28, 0x158080
	v_lshl_add_u64 v[174:175], v[176:177], 0, s[12:13]
	s_addc_u32 s25, s29, 0
	s_add_i32 s28, s60, s3
	global_load_lds_dwordx4 v[174:175], off
	v_lshl_add_u64 v[174:175], s[24:25], 0, v[164:165]
	s_mov_b32 m0, s28
	s_nop 0
	global_load_lds_dwordx4 v[174:175], off
	v_lshl_add_u64 v[174:175], s[24:25], 0, v[162:163]
	s_add_i32 m0, s28, 0x2000
	s_nop 0
	global_load_lds_dwordx4 v[174:175], off
	v_lshl_add_u64 v[174:175], v[178:179], 0, s[12:13]
	s_mov_b32 m0, s38
	s_nop 0
	global_load_lds_dwordx4 v[174:175], off
	v_lshl_add_u64 v[174:175], v[180:181], 0, s[12:13]
	s_mov_b32 m0, s39
	s_nop 0
	global_load_lds_dwordx4 v[174:175], off
	s_waitcnt vmcnt(8)
	s_waitcnt lgkmcnt(0)
	s_barrier
	s_setprio 1
	s_waitcnt lgkmcnt(0)
	v_mfma_scale_f32_16x16x128_f8f6f4 v[62:65], v[2:9], v[204:211], v[62:65], v1, v1 op_sel_hi:[0,0,0]
	v_mfma_scale_f32_16x16x128_f8f6f4 v[58:61], v[10:17], v[204:211], v[58:61], v1, v1 op_sel_hi:[0,0,0]
	v_mfma_scale_f32_16x16x128_f8f6f4 v[90:93], v[10:17], v[188:195], v[90:93], v1, v1 op_sel_hi:[0,0,0]
	v_mfma_scale_f32_16x16x128_f8f6f4 v[94:97], v[2:9], v[188:195], v[94:97], v1, v1 op_sel_hi:[0,0,0]
	v_mfma_scale_f32_16x16x128_f8f6f4 v[78:81], v[2:9], v[196:203], v[78:81], v1, v1 op_sel_hi:[0,0,0]
	v_mfma_scale_f32_16x16x128_f8f6f4 v[74:77], v[10:17], v[196:203], v[74:77], v1, v1 op_sel_hi:[0,0,0]
	v_mfma_scale_f32_16x16x128_f8f6f4 v[42:45], v[10:17], v[212:219], v[42:45], v1, v1 op_sel_hi:[0,0,0]
	v_mfma_scale_f32_16x16x128_f8f6f4 v[46:49], v[2:9], v[212:219], v[46:49], v1, v1 op_sel_hi:[0,0,0]
	s_setprio 0
	s_setprio 1
	v_mfma_scale_f32_16x16x128_f8f6f4 v[38:41], v[18:25], v[212:219], v[38:41], v1, v1 op_sel_hi:[0,0,0]
	v_mfma_scale_f32_16x16x128_f8f6f4 v[34:37], v[26:33], v[212:219], v[34:37], v1, v1 op_sel_hi:[0,0,0]
	v_mfma_scale_f32_16x16x128_f8f6f4 v[82:85], v[26:33], v[188:195], v[82:85], v1, v1 op_sel_hi:[0,0,0]
	v_mfma_scale_f32_16x16x128_f8f6f4 v[86:89], v[18:25], v[188:195], v[86:89], v1, v1 op_sel_hi:[0,0,0]
	v_mfma_scale_f32_16x16x128_f8f6f4 v[70:73], v[18:25], v[196:203], v[70:73], v1, v1 op_sel_hi:[0,0,0]
	v_mfma_scale_f32_16x16x128_f8f6f4 v[66:69], v[26:33], v[196:203], v[66:69], v1, v1 op_sel_hi:[0,0,0]
	v_mfma_scale_f32_16x16x128_f8f6f4 v[50:53], v[26:33], v[204:211], v[50:53], v1, v1 op_sel_hi:[0,0,0]
	v_mfma_scale_f32_16x16x128_f8f6f4 v[54:57], v[18:25], v[204:211], v[54:57], v1, v1 op_sel_hi:[0,0,0]
	s_setprio 0
	s_barrier
	s_add_i32 s58, s58, 2
	s_add_u32 s26, s26, 0x100
	s_addc_u32 s27, s27, 0
	s_add_u32 s50, s50, 0x100
	s_addc_u32 s51, s51, 0
	s_cmpk_gt_u32 s58, 0x53
	s_cbranch_scc0 .LBB0_318
	s_and_b64 vcc, exec, s[14:15]
	s_cbranch_vccz .LBB0_321
	s_barrier

.LBB0_332:
	s_add_u32 s6, s61, s4
	s_addc_u32 s7, s62, s5
	s_add_u32 s6, s6, 0x32800100
	s_addc_u32 s7, s7, 0
	s_add_u32 s24, s63, s4
	s_addc_u32 s25, s68, s5
	s_add_i32 s64, 0, 0x10000
	s_cmpk_eq_i32 s4, 0x2a00
	s_cselect_b32 s13, s1, s7
	s_cselect_b32 s12, s0, s6
	s_cselect_b32 s7, s29, s25
	s_cselect_b32 s6, s28, s24
	s_add_i32 s65, 0, 0x14000
	v_add_u32_e32 v2, s64, v188
	v_add_u32_e32 v6, s65, v188
	ds_read_b128 v[26:29], v2
	ds_read_b128 v[30:33], v2 offset:1024
	ds_read_b128 v[18:21], v2 offset:2048
	ds_read_b128 v[22:25], v2 offset:3072
	ds_read_b128 v[10:13], v6
	ds_read_b128 v[14:17], v6 offset:1024
	ds_read_b128 v[2:5], v6 offset:2048
	ds_read_b128 v[6:9], v6 offset:3072
	v_lshl_add_u64 v[214:215], v[168:169], 0, s[4:5]
	s_add_i32 m0, s18, 0xc000
	ds_read_b128 v[172:175], v189
	ds_read_b128 v[176:179], v189 offset:1024
	ds_read_b128 v[190:193], v189 offset:2048
	ds_read_b128 v[194:197], v189 offset:3072
	ds_read_b128 v[198:201], v189 offset:4096
	ds_read_b128 v[202:205], v189 offset:5120
	ds_read_b128 v[206:209], v189 offset:6144
	ds_read_b128 v[210:213], v189 offset:7168
	global_load_lds_dwordx4 v[214:215], off
	v_lshl_add_u64 v[214:215], v[170:171], 0, s[4:5]
	s_add_i32 m0, s18, 0xe000
	s_nop 0
	global_load_lds_dwordx4 v[214:215], off
	s_waitcnt vmcnt(8)
	s_waitcnt lgkmcnt(0)
	s_barrier
	s_setprio 1
	s_waitcnt lgkmcnt(0)
	v_mfma_scale_f32_16x16x128_f8f6f4 v[70:73], v[26:33], v[172:179], v[70:73], v187, v187 op_sel_hi:[0,0,0]
	v_mfma_scale_f32_16x16x128_f8f6f4 v[66:69], v[18:25], v[172:179], v[66:69], v187, v187 op_sel_hi:[0,0,0]
	v_mfma_scale_f32_16x16x128_f8f6f4 v[74:77], v[18:25], v[190:197], v[74:77], v187, v187 op_sel_hi:[0,0,0]
	v_mfma_scale_f32_16x16x128_f8f6f4 v[78:81], v[26:33], v[190:197], v[78:81], v187, v187 op_sel_hi:[0,0,0]
	v_mfma_scale_f32_16x16x128_f8f6f4 v[86:89], v[26:33], v[198:205], v[86:89], v187, v187 op_sel_hi:[0,0,0]
	v_mfma_scale_f32_16x16x128_f8f6f4 v[82:85], v[18:25], v[198:205], v[82:85], v187, v187 op_sel_hi:[0,0,0]
	v_mfma_scale_f32_16x16x128_f8f6f4 v[90:93], v[18:25], v[206:213], v[90:93], v187, v187 op_sel_hi:[0,0,0]
	v_mfma_scale_f32_16x16x128_f8f6f4 v[94:97], v[26:33], v[206:213], v[94:97], v187, v187 op_sel_hi:[0,0,0]
	s_setprio 0
	s_setprio 1
	v_mfma_scale_f32_16x16x128_f8f6f4 v[134:137], v[10:17], v[206:213], v[134:137], v187, v187 op_sel_hi:[0,0,0]
	v_mfma_scale_f32_16x16x128_f8f6f4 v[130:133], v[2:9], v[206:213], v[130:133], v187, v187 op_sel_hi:[0,0,0]
	v_mfma_scale_f32_16x16x128_f8f6f4 v[154:157], v[2:9], v[172:179], v[154:157], v187, v187 op_sel_hi:[0,0,0]
	v_mfma_scale_f32_16x16x128_f8f6f4 v[158:161], v[10:17], v[172:179], v[158:161], v187, v187 op_sel_hi:[0,0,0]
	v_mfma_scale_f32_16x16x128_f8f6f4 v[150:153], v[10:17], v[190:197], v[150:153], v187, v187 op_sel_hi:[0,0,0]
	v_mfma_scale_f32_16x16x128_f8f6f4 v[146:149], v[2:9], v[190:197], v[146:149], v187, v187 op_sel_hi:[0,0,0]
	v_mfma_scale_f32_16x16x128_f8f6f4 v[138:141], v[2:9], v[198:205], v[138:141], v187, v187 op_sel_hi:[0,0,0]
	v_mfma_scale_f32_16x16x128_f8f6f4 v[142:145], v[10:17], v[198:205], v[142:145], v187, v187 op_sel_hi:[0,0,0]
	s_setprio 0
	s_barrier
	s_add_i32 s24, s64, s17
	v_lshl_add_u64 v[172:173], s[6:7], 0, v[162:163]
	s_mov_b32 m0, s24
	ds_read_b128 v[190:193], v189 offset:16384
	ds_read_b128 v[194:197], v189 offset:17408
	ds_read_b128 v[198:201], v189 offset:18432
	ds_read_b128 v[202:205], v189 offset:19456
	ds_read_b128 v[206:209], v189 offset:20480
	ds_read_b128 v[210:213], v189 offset:21504
	ds_read_b128 v[214:217], v189 offset:22528
	ds_read_b128 v[218:221], v189 offset:23552
	global_load_lds_dwordx4 v[172:173], off
	s_add_i32 m0, s24, 0x2000
	s_add_u32 s24, s6, 0x158000
	v_lshl_add_u64 v[174:175], s[6:7], 0, v[166:167]
	s_addc_u32 s25, s7, 0
	s_add_i32 s64, s65, s17
	global_load_lds_dwordx4 v[174:175], off
	v_lshl_add_u64 v[176:177], s[24:25], 0, v[162:163]
	s_mov_b32 m0, s64
	v_lshl_add_u64 v[178:179], s[12:13], 0, v[166:167]
	global_load_lds_dwordx4 v[176:177], off
	v_lshl_add_u64 v[176:177], s[24:25], 0, v[166:167]
	s_add_i32 m0, s64, 0x2000
	s_nop 0
	global_load_lds_dwordx4 v[176:177], off
	v_lshl_add_u64 v[176:177], s[12:13], 0, v[162:163]
	s_mov_b32 m0, s18
	s_nop 0
	global_load_lds_dwordx4 v[176:177], off
	s_mov_b32 m0, s19
	s_nop 0
	global_load_lds_dwordx4 v[178:179], off
	s_waitcnt vmcnt(8)
	s_waitcnt lgkmcnt(0)
	s_barrier
	s_setprio 1
	s_waitcnt lgkmcnt(0)
	v_mfma_scale_f32_16x16x128_f8f6f4 v[110:113], v[26:33], v[198:205], v[110:113], v187, v187 op_sel_hi:[0,0,0]
	v_mfma_scale_f32_16x16x128_f8f6f4 v[106:109], v[18:25], v[198:205], v[106:109], v187, v187 op_sel_hi:[0,0,0]
	v_mfma_scale_f32_16x16x128_f8f6f4 v[98:101], v[18:25], v[190:197], v[98:101], v187, v187 op_sel_hi:[0,0,0]
	v_mfma_scale_f32_16x16x128_f8f6f4 v[102:105], v[26:33], v[190:197], v[102:105], v187, v187 op_sel_hi:[0,0,0]
	v_mfma_scale_f32_16x16x128_f8f6f4 v[118:121], v[26:33], v[206:213], v[118:121], v187, v187 op_sel_hi:[0,0,0]
	v_mfma_scale_f32_16x16x128_f8f6f4 v[114:117], v[18:25], v[206:213], v[114:117], v187, v187 op_sel_hi:[0,0,0]
	v_mfma_scale_f32_16x16x128_f8f6f4 v[122:125], v[18:25], v[214:221], v[122:125], v187, v187 op_sel_hi:[0,0,0]
	v_mfma_scale_f32_16x16x128_f8f6f4 v[126:129], v[26:33], v[214:221], v[126:129], v187, v187 op_sel_hi:[0,0,0]
	s_setprio 0
	s_setprio 1
	v_mfma_scale_f32_16x16x128_f8f6f4 v[62:65], v[10:17], v[214:221], v[62:65], v187, v187 op_sel_hi:[0,0,0]
	v_mfma_scale_f32_16x16x128_f8f6f4 v[58:61], v[2:9], v[214:221], v[58:61], v187, v187 op_sel_hi:[0,0,0]
	v_mfma_scale_f32_16x16x128_f8f6f4 v[34:37], v[2:9], v[190:197], v[34:37], v187, v187 op_sel_hi:[0,0,0]
	v_mfma_scale_f32_16x16x128_f8f6f4 v[38:41], v[10:17], v[190:197], v[38:41], v187, v187 op_sel_hi:[0,0,0]
	v_mfma_scale_f32_16x16x128_f8f6f4 v[46:49], v[10:17], v[198:205], v[46:49], v187, v187 op_sel_hi:[0,0,0]
	v_mfma_scale_f32_16x16x128_f8f6f4 v[42:45], v[2:9], v[198:205], v[42:45], v187, v187 op_sel_hi:[0,0,0]
	v_mfma_scale_f32_16x16x128_f8f6f4 v[50:53], v[2:9], v[206:213], v[50:53], v187, v187 op_sel_hi:[0,0,0]
	v_mfma_scale_f32_16x16x128_f8f6f4 v[54:57], v[10:17], v[206:213], v[54:57], v187, v187 op_sel_hi:[0,0,0]
	s_setprio 0
	s_barrier
	s_add_i32 s24, 0, 0x18000
	s_add_i32 s25, 0, 0x1c000
	v_add_u32_e32 v14, s24, v188
	v_add_u32_e32 v30, s25, v188
	ds_read_b128 v[2:5], v14
	ds_read_b128 v[6:9], v14 offset:1024
	ds_read_b128 v[10:13], v14 offset:2048
	ds_read_b128 v[14:17], v14 offset:3072
	ds_read_b128 v[18:21], v30
	ds_read_b128 v[22:25], v30 offset:1024
	ds_read_b128 v[26:29], v30 offset:2048
	ds_read_b128 v[30:33], v30 offset:3072
	s_add_u32 s12, s12, 0x158000
	s_addc_u32 s13, s13, 0
	s_mov_b32 m0, s93
	v_lshl_add_u64 v[222:223], s[12:13], 0, v[162:163]
	ds_read_b128 v[190:193], v189 offset:32768
	ds_read_b128 v[194:197], v189 offset:33792
	ds_read_b128 v[198:201], v189 offset:34816
	ds_read_b128 v[202:205], v189 offset:35840
	ds_read_b128 v[206:209], v189 offset:36864
	ds_read_b128 v[210:213], v189 offset:37888
	ds_read_b128 v[214:217], v189 offset:38912
	ds_read_b128 v[218:221], v189 offset:39936
	global_load_lds_dwordx4 v[222:223], off
	v_lshl_add_u64 v[222:223], s[12:13], 0, v[166:167]
	s_mov_b32 m0, s94
	s_nop 0
	global_load_lds_dwordx4 v[222:223], off
	s_waitcnt vmcnt(8)
	s_waitcnt lgkmcnt(0)
	s_barrier
	s_setprio 1
	s_waitcnt lgkmcnt(0)
	v_mfma_scale_f32_16x16x128_f8f6f4 v[82:85], v[10:17], v[206:213], v[82:85], v187, v187 op_sel_hi:[0,0,0]
	v_mfma_scale_f32_16x16x128_f8f6f4 v[86:89], v[2:9], v[206:213], v[86:89], v187, v187 op_sel_hi:[0,0,0]
	v_mfma_scale_f32_16x16x128_f8f6f4 v[70:73], v[2:9], v[190:197], v[70:73], v187, v187 op_sel_hi:[0,0,0]
	v_mfma_scale_f32_16x16x128_f8f6f4 v[66:69], v[10:17], v[190:197], v[66:69], v187, v187 op_sel_hi:[0,0,0]
	v_mfma_scale_f32_16x16x128_f8f6f4 v[74:77], v[10:17], v[198:205], v[74:77], v187, v187 op_sel_hi:[0,0,0]
	v_mfma_scale_f32_16x16x128_f8f6f4 v[78:81], v[2:9], v[198:205], v[78:81], v187, v187 op_sel_hi:[0,0,0]
	v_mfma_scale_f32_16x16x128_f8f6f4 v[94:97], v[2:9], v[214:221], v[94:97], v187, v187 op_sel_hi:[0,0,0]
	v_mfma_scale_f32_16x16x128_f8f6f4 v[90:93], v[10:17], v[214:221], v[90:93], v187, v187 op_sel_hi:[0,0,0]
	s_setprio 0
	s_setprio 1
	v_mfma_scale_f32_16x16x128_f8f6f4 v[134:137], v[18:25], v[214:221], v[134:137], v187, v187 op_sel_hi:[0,0,0]
	v_mfma_scale_f32_16x16x128_f8f6f4 v[130:133], v[26:33], v[214:221], v[130:133], v187, v187 op_sel_hi:[0,0,0]
	v_mfma_scale_f32_16x16x128_f8f6f4 v[154:157], v[26:33], v[190:197], v[154:157], v187, v187 op_sel_hi:[0,0,0]
	v_mfma_scale_f32_16x16x128_f8f6f4 v[158:161], v[18:25], v[190:197], v[158:161], v187, v187 op_sel_hi:[0,0,0]
	v_mfma_scale_f32_16x16x128_f8f6f4 v[150:153], v[18:25], v[198:205], v[150:153], v187, v187 op_sel_hi:[0,0,0]
	v_mfma_scale_f32_16x16x128_f8f6f4 v[146:149], v[26:33], v[198:205], v[146:149], v187, v187 op_sel_hi:[0,0,0]
	v_mfma_scale_f32_16x16x128_f8f6f4 v[138:141], v[26:33], v[206:213], v[138:141], v187, v187 op_sel_hi:[0,0,0]
	v_mfma_scale_f32_16x16x128_f8f6f4 v[142:145], v[18:25], v[206:213], v[142:145], v187, v187 op_sel_hi:[0,0,0]
	s_setprio 0
	s_barrier
	s_add_i32 s12, s24, s17
	v_lshl_add_u64 v[172:173], v[172:173], 0, s[76:77]
	s_mov_b32 m0, s12
	ds_read_b128 v[190:193], v189 offset:49152
	ds_read_b128 v[194:197], v189 offset:50176
	ds_read_b128 v[198:201], v189 offset:51200
	ds_read_b128 v[202:205], v189 offset:52224
	ds_read_b128 v[206:209], v189 offset:53248
	ds_read_b128 v[210:213], v189 offset:54272
	ds_read_b128 v[214:217], v189 offset:55296
	ds_read_b128 v[218:221], v189 offset:56320
	global_load_lds_dwordx4 v[172:173], off
	s_add_i32 m0, s12, 0x2000
	s_add_u32 s6, s6, 0x158080
	v_lshl_add_u64 v[172:173], v[174:175], 0, s[76:77]
	s_addc_u32 s7, s7, 0
	s_add_i32 s12, s25, s17
	global_load_lds_dwordx4 v[172:173], off
	v_lshl_add_u64 v[172:173], s[6:7], 0, v[162:163]
	s_mov_b32 m0, s12
	s_nop 0
	global_load_lds_dwordx4 v[172:173], off
	v_lshl_add_u64 v[172:173], s[6:7], 0, v[166:167]
	s_add_i32 m0, s12, 0x2000
	s_nop 0
	global_load_lds_dwordx4 v[172:173], off
	v_lshl_add_u64 v[172:173], v[176:177], 0, s[76:77]
	s_mov_b32 m0, s95
	s_nop 0
	global_load_lds_dwordx4 v[172:173], off
	v_lshl_add_u64 v[172:173], v[178:179], 0, s[76:77]
	s_mov_b32 m0, vcc_lo
	s_nop 0
	global_load_lds_dwordx4 v[172:173], off
	s_waitcnt vmcnt(8)
	s_waitcnt lgkmcnt(0)
	s_barrier
	s_setprio 1
	s_waitcnt lgkmcnt(0)
	v_mfma_scale_f32_16x16x128_f8f6f4 v[118:121], v[2:9], v[206:213], v[118:121], v187, v187 op_sel_hi:[0,0,0]
	v_mfma_scale_f32_16x16x128_f8f6f4 v[114:117], v[10:17], v[206:213], v[114:117], v187, v187 op_sel_hi:[0,0,0]
	v_mfma_scale_f32_16x16x128_f8f6f4 v[98:101], v[10:17], v[190:197], v[98:101], v187, v187 op_sel_hi:[0,0,0]
	v_mfma_scale_f32_16x16x128_f8f6f4 v[102:105], v[2:9], v[190:197], v[102:105], v187, v187 op_sel_hi:[0,0,0]
	v_mfma_scale_f32_16x16x128_f8f6f4 v[110:113], v[2:9], v[198:205], v[110:113], v187, v187 op_sel_hi:[0,0,0]
	v_mfma_scale_f32_16x16x128_f8f6f4 v[106:109], v[10:17], v[198:205], v[106:109], v187, v187 op_sel_hi:[0,0,0]
	v_mfma_scale_f32_16x16x128_f8f6f4 v[122:125], v[10:17], v[214:221], v[122:125], v187, v187 op_sel_hi:[0,0,0]
	v_mfma_scale_f32_16x16x128_f8f6f4 v[126:129], v[2:9], v[214:221], v[126:129], v187, v187 op_sel_hi:[0,0,0]
	s_setprio 0
	s_setprio 1
	v_mfma_scale_f32_16x16x128_f8f6f4 v[62:65], v[18:25], v[214:221], v[62:65], v187, v187 op_sel_hi:[0,0,0]
	v_mfma_scale_f32_16x16x128_f8f6f4 v[58:61], v[26:33], v[214:221], v[58:61], v187, v187 op_sel_hi:[0,0,0]
	v_mfma_scale_f32_16x16x128_f8f6f4 v[34:37], v[26:33], v[190:197], v[34:37], v187, v187 op_sel_hi:[0,0,0]
	v_mfma_scale_f32_16x16x128_f8f6f4 v[38:41], v[18:25], v[190:197], v[38:41], v187, v187 op_sel_hi:[0,0,0]
	v_mfma_scale_f32_16x16x128_f8f6f4 v[46:49], v[18:25], v[198:205], v[46:49], v187, v187 op_sel_hi:[0,0,0]
	v_mfma_scale_f32_16x16x128_f8f6f4 v[42:45], v[26:33], v[198:205], v[42:45], v187, v187 op_sel_hi:[0,0,0]
	v_mfma_scale_f32_16x16x128_f8f6f4 v[50:53], v[26:33], v[206:213], v[50:53], v187, v187 op_sel_hi:[0,0,0]
	v_mfma_scale_f32_16x16x128_f8f6f4 v[54:57], v[18:25], v[206:213], v[54:57], v187, v187 op_sel_hi:[0,0,0]
	s_setprio 0
	s_barrier
	s_add_i32 vcc_hi, vcc_hi, 2
	s_add_u32 s4, s4, 0x100
	s_addc_u32 s5, s5, 0
	s_cmpk_lt_u32 vcc_hi, 0x54
	s_cbranch_scc1 .LBB0_332
	s_waitcnt vmcnt(0)
	s_mov_b64 s[12:13], s[54:55]
	s_cmpk_gt_u32 s89, 0xff
	s_cbranch_scc1 .LBB0_335
	s_barrier

.LBB0_1291:
	ds_read_b128 v[26:29], v184
	ds_read_b128 v[30:33], v184 offset:1024
	ds_read_b128 v[18:21], v184 offset:2048
	ds_read_b128 v[22:25], v184 offset:3072
	ds_read_b128 v[10:13], v185
	ds_read_b128 v[14:17], v185 offset:1024
	ds_read_b128 v[2:5], v185 offset:2048
	ds_read_b128 v[6:9], v185 offset:3072
	s_add_u32 s20, s14, s16
	s_addc_u32 s21, s15, s17
	s_add_u32 s20, s20, 0x2a800100
	s_addc_u32 s21, s21, 0
	s_add_u32 s48, s31, s16
	s_addc_u32 s49, s34, s17
	s_cmpk_eq_i32 s16, 0x700
	s_cselect_b32 s23, s9, s21
	s_cselect_b32 s22, s8, s20
	s_cselect_b32 s21, s5, s49
	s_cselect_b32 s20, s4, s48
	s_mov_b32 m0, s36
	v_lshl_add_u64 v[214:215], v[170:171], 0, s[16:17]
	ds_read_b128 v[174:177], v186
	ds_read_b128 v[178:181], v186 offset:1024
	ds_read_b128 v[190:193], v186 offset:2048
	ds_read_b128 v[194:197], v186 offset:3072
	ds_read_b128 v[198:201], v186 offset:4096
	ds_read_b128 v[202:205], v186 offset:5120
	ds_read_b128 v[206:209], v186 offset:6144
	ds_read_b128 v[210:213], v186 offset:7168
	global_load_lds_dwordx4 v[214:215], off
	v_lshl_add_u64 v[214:215], v[172:173], 0, s[16:17]
	s_mov_b32 m0, s37
	s_nop 0
	global_load_lds_dwordx4 v[214:215], off
	s_waitcnt vmcnt(8)
	s_waitcnt lgkmcnt(0)
	s_barrier
	s_setprio 1
	s_waitcnt lgkmcnt(0)
	v_mfma_scale_f32_16x16x128_f8f6f4 v[158:161], v[26:33], v[174:181], v[158:161], v1, v1 op_sel_hi:[0,0,0]
	v_mfma_scale_f32_16x16x128_f8f6f4 v[154:157], v[18:25], v[174:181], v[154:157], v1, v1 op_sel_hi:[0,0,0]
	v_mfma_scale_f32_16x16x128_f8f6f4 v[138:141], v[18:25], v[190:197], v[138:141], v1, v1 op_sel_hi:[0,0,0]
	v_mfma_scale_f32_16x16x128_f8f6f4 v[146:149], v[26:33], v[190:197], v[146:149], v1, v1 op_sel_hi:[0,0,0]
	v_mfma_scale_f32_16x16x128_f8f6f4 v[130:133], v[26:33], v[198:205], v[130:133], v1, v1 op_sel_hi:[0,0,0]
	v_mfma_scale_f32_16x16x128_f8f6f4 v[122:125], v[18:25], v[198:205], v[122:125], v1, v1 op_sel_hi:[0,0,0]
	v_mfma_scale_f32_16x16x128_f8f6f4 v[106:109], v[18:25], v[206:213], v[106:109], v1, v1 op_sel_hi:[0,0,0]
	v_mfma_scale_f32_16x16x128_f8f6f4 v[114:117], v[26:33], v[206:213], v[114:117], v1, v1 op_sel_hi:[0,0,0]
	s_setprio 0
	s_setprio 1
	v_mfma_scale_f32_16x16x128_f8f6f4 v[102:105], v[10:17], v[206:213], v[102:105], v1, v1 op_sel_hi:[0,0,0]
	v_mfma_scale_f32_16x16x128_f8f6f4 v[98:101], v[2:9], v[206:213], v[98:101], v1, v1 op_sel_hi:[0,0,0]
	v_mfma_scale_f32_16x16x128_f8f6f4 v[142:145], v[2:9], v[174:181], v[142:145], v1, v1 op_sel_hi:[0,0,0]
	v_mfma_scale_f32_16x16x128_f8f6f4 v[150:153], v[10:17], v[174:181], v[150:153], v1, v1 op_sel_hi:[0,0,0]
	v_mfma_scale_f32_16x16x128_f8f6f4 v[134:137], v[10:17], v[190:197], v[134:137], v1, v1 op_sel_hi:[0,0,0]
	v_mfma_scale_f32_16x16x128_f8f6f4 v[126:129], v[2:9], v[190:197], v[126:129], v1, v1 op_sel_hi:[0,0,0]
	v_mfma_scale_f32_16x16x128_f8f6f4 v[110:113], v[2:9], v[198:205], v[110:113], v1, v1 op_sel_hi:[0,0,0]
	v_mfma_scale_f32_16x16x128_f8f6f4 v[118:121], v[10:17], v[198:205], v[118:121], v1, v1 op_sel_hi:[0,0,0]
	s_setprio 0
	s_barrier
	s_mov_b32 m0, s38
	v_lshl_add_u64 v[174:175], s[20:21], 0, v[164:165]
	s_add_u32 s48, s20, 0x80000
	ds_read_b128 v[190:193], v186 offset:16384
	ds_read_b128 v[194:197], v186 offset:17408
	ds_read_b128 v[198:201], v186 offset:18432
	ds_read_b128 v[202:205], v186 offset:19456
	ds_read_b128 v[206:209], v186 offset:20480
	ds_read_b128 v[210:213], v186 offset:21504
	ds_read_b128 v[214:217], v186 offset:22528
	ds_read_b128 v[218:221], v186 offset:23552
	global_load_lds_dwordx4 v[174:175], off
	v_lshl_add_u64 v[176:177], s[20:21], 0, v[168:169]
	s_mov_b32 m0, s39
	s_addc_u32 s49, s21, 0
	global_load_lds_dwordx4 v[176:177], off
	v_lshl_add_u64 v[178:179], s[48:49], 0, v[164:165]
	s_mov_b32 m0, s40
	v_lshl_add_u64 v[180:181], s[22:23], 0, v[166:167]
	global_load_lds_dwordx4 v[178:179], off
	v_lshl_add_u64 v[178:179], s[48:49], 0, v[168:169]
	s_mov_b32 m0, s41
	s_nop 0
	global_load_lds_dwordx4 v[178:179], off
	v_lshl_add_u64 v[178:179], s[22:23], 0, v[162:163]
	s_mov_b32 m0, s24
	s_nop 0
	global_load_lds_dwordx4 v[178:179], off
	s_mov_b32 m0, s25
	s_nop 0
	global_load_lds_dwordx4 v[180:181], off
	s_waitcnt vmcnt(8)
	s_waitcnt lgkmcnt(0)
	s_barrier
	s_setprio 1
	s_waitcnt lgkmcnt(0)
	v_mfma_scale_f32_16x16x128_f8f6f4 v[82:85], v[26:33], v[198:205], v[82:85], v1, v1 op_sel_hi:[0,0,0]
	v_mfma_scale_f32_16x16x128_f8f6f4 v[74:77], v[18:25], v[198:205], v[74:77], v1, v1 op_sel_hi:[0,0,0]
	v_mfma_scale_f32_16x16x128_f8f6f4 v[90:93], v[18:25], v[190:197], v[90:93], v1, v1 op_sel_hi:[0,0,0]
	v_mfma_scale_f32_16x16x128_f8f6f4 v[94:97], v[26:33], v[190:197], v[94:97], v1, v1 op_sel_hi:[0,0,0]
	v_mfma_scale_f32_16x16x128_f8f6f4 v[66:69], v[26:33], v[206:213], v[66:69], v1, v1 op_sel_hi:[0,0,0]
	v_mfma_scale_f32_16x16x128_f8f6f4 v[58:61], v[18:25], v[206:213], v[58:61], v1, v1 op_sel_hi:[0,0,0]
	v_mfma_scale_f32_16x16x128_f8f6f4 v[42:45], v[18:25], v[214:221], v[42:45], v1, v1 op_sel_hi:[0,0,0]
	v_mfma_scale_f32_16x16x128_f8f6f4 v[50:53], v[26:33], v[214:221], v[50:53], v1, v1 op_sel_hi:[0,0,0]
	s_setprio 0
	s_setprio 1
	v_mfma_scale_f32_16x16x128_f8f6f4 v[38:41], v[10:17], v[214:221], v[38:41], v1, v1 op_sel_hi:[0,0,0]
	v_mfma_scale_f32_16x16x128_f8f6f4 v[34:37], v[2:9], v[214:221], v[34:37], v1, v1 op_sel_hi:[0,0,0]
	v_mfma_scale_f32_16x16x128_f8f6f4 v[78:81], v[2:9], v[190:197], v[78:81], v1, v1 op_sel_hi:[0,0,0]
	v_mfma_scale_f32_16x16x128_f8f6f4 v[86:89], v[10:17], v[190:197], v[86:89], v1, v1 op_sel_hi:[0,0,0]
	v_mfma_scale_f32_16x16x128_f8f6f4 v[70:73], v[10:17], v[198:205], v[70:73], v1, v1 op_sel_hi:[0,0,0]
	v_mfma_scale_f32_16x16x128_f8f6f4 v[62:65], v[2:9], v[198:205], v[62:65], v1, v1 op_sel_hi:[0,0,0]
	v_mfma_scale_f32_16x16x128_f8f6f4 v[46:49], v[2:9], v[206:213], v[46:49], v1, v1 op_sel_hi:[0,0,0]
	v_mfma_scale_f32_16x16x128_f8f6f4 v[54:57], v[10:17], v[206:213], v[54:57], v1, v1 op_sel_hi:[0,0,0]
	s_setprio 0
	s_barrier
	ds_read_b128 v[2:5], v187
	ds_read_b128 v[6:9], v187 offset:1024
	ds_read_b128 v[10:13], v187 offset:2048
	ds_read_b128 v[14:17], v187 offset:3072
	ds_read_b128 v[18:21], v188
	ds_read_b128 v[22:25], v188 offset:1024
	ds_read_b128 v[26:29], v188 offset:2048
	ds_read_b128 v[30:33], v188 offset:3072
	s_add_u32 s22, s22, 0x80000
	s_addc_u32 s23, s23, 0
	s_mov_b32 m0, s26
	v_lshl_add_u64 v[222:223], s[22:23], 0, v[162:163]
	ds_read_b128 v[190:193], v186 offset:32768
	ds_read_b128 v[194:197], v186 offset:33792
	ds_read_b128 v[198:201], v186 offset:34816
	ds_read_b128 v[202:205], v186 offset:35840
	ds_read_b128 v[206:209], v186 offset:36864
	ds_read_b128 v[210:213], v186 offset:37888
	ds_read_b128 v[214:217], v186 offset:38912
	ds_read_b128 v[218:221], v186 offset:39936
	global_load_lds_dwordx4 v[222:223], off
	v_lshl_add_u64 v[222:223], s[22:23], 0, v[166:167]
	s_mov_b32 m0, s27
	s_nop 0
	global_load_lds_dwordx4 v[222:223], off
	s_waitcnt vmcnt(8)
	s_waitcnt lgkmcnt(0)
	s_barrier
	s_setprio 1
	s_waitcnt lgkmcnt(0)
	v_mfma_scale_f32_16x16x128_f8f6f4 v[122:125], v[10:17], v[206:213], v[122:125], v1, v1 op_sel_hi:[0,0,0]
	v_mfma_scale_f32_16x16x128_f8f6f4 v[130:133], v[2:9], v[206:213], v[130:133], v1, v1 op_sel_hi:[0,0,0]
	v_mfma_scale_f32_16x16x128_f8f6f4 v[158:161], v[2:9], v[190:197], v[158:161], v1, v1 op_sel_hi:[0,0,0]
	v_mfma_scale_f32_16x16x128_f8f6f4 v[154:157], v[10:17], v[190:197], v[154:157], v1, v1 op_sel_hi:[0,0,0]
	v_mfma_scale_f32_16x16x128_f8f6f4 v[138:141], v[10:17], v[198:205], v[138:141], v1, v1 op_sel_hi:[0,0,0]
	v_mfma_scale_f32_16x16x128_f8f6f4 v[146:149], v[2:9], v[198:205], v[146:149], v1, v1 op_sel_hi:[0,0,0]
	v_mfma_scale_f32_16x16x128_f8f6f4 v[114:117], v[2:9], v[214:221], v[114:117], v1, v1 op_sel_hi:[0,0,0]
	v_mfma_scale_f32_16x16x128_f8f6f4 v[106:109], v[10:17], v[214:221], v[106:109], v1, v1 op_sel_hi:[0,0,0]
	s_setprio 0
	s_setprio 1
	v_mfma_scale_f32_16x16x128_f8f6f4 v[102:105], v[18:25], v[214:221], v[102:105], v1, v1 op_sel_hi:[0,0,0]
	v_mfma_scale_f32_16x16x128_f8f6f4 v[98:101], v[26:33], v[214:221], v[98:101], v1, v1 op_sel_hi:[0,0,0]
	v_mfma_scale_f32_16x16x128_f8f6f4 v[142:145], v[26:33], v[190:197], v[142:145], v1, v1 op_sel_hi:[0,0,0]
	v_mfma_scale_f32_16x16x128_f8f6f4 v[150:153], v[18:25], v[190:197], v[150:153], v1, v1 op_sel_hi:[0,0,0]
	v_mfma_scale_f32_16x16x128_f8f6f4 v[134:137], v[18:25], v[198:205], v[134:137], v1, v1 op_sel_hi:[0,0,0]
	v_mfma_scale_f32_16x16x128_f8f6f4 v[126:129], v[26:33], v[198:205], v[126:129], v1, v1 op_sel_hi:[0,0,0]
	v_mfma_scale_f32_16x16x128_f8f6f4 v[110:113], v[26:33], v[206:213], v[110:113], v1, v1 op_sel_hi:[0,0,0]
	v_mfma_scale_f32_16x16x128_f8f6f4 v[118:121], v[18:25], v[206:213], v[118:121], v1, v1 op_sel_hi:[0,0,0]
	s_setprio 0
	s_barrier
	s_mov_b32 m0, s42
	v_lshl_add_u64 v[174:175], v[174:175], 0, s[12:13]
	s_add_u32 s20, s20, 0x80080
	ds_read_b128 v[190:193], v186 offset:49152
	ds_read_b128 v[194:197], v186 offset:50176
	ds_read_b128 v[198:201], v186 offset:51200
	ds_read_b128 v[202:205], v186 offset:52224
	ds_read_b128 v[206:209], v186 offset:53248
	ds_read_b128 v[210:213], v186 offset:54272
	ds_read_b128 v[214:217], v186 offset:55296
	ds_read_b128 v[218:221], v186 offset:56320
	global_load_lds_dwordx4 v[174:175], off
	v_lshl_add_u64 v[174:175], v[176:177], 0, s[12:13]
	s_mov_b32 m0, s43
	s_addc_u32 s21, s21, 0
	global_load_lds_dwordx4 v[174:175], off
	v_lshl_add_u64 v[174:175], s[20:21], 0, v[164:165]
	s_mov_b32 m0, s44
	s_nop 0
	global_load_lds_dwordx4 v[174:175], off
	v_lshl_add_u64 v[174:175], s[20:21], 0, v[168:169]
	s_mov_b32 m0, s45
	s_nop 0
	global_load_lds_dwordx4 v[174:175], off
	v_lshl_add_u64 v[174:175], v[178:179], 0, s[12:13]
	s_mov_b32 m0, s29
	s_nop 0
	global_load_lds_dwordx4 v[174:175], off
	v_lshl_add_u64 v[174:175], v[180:181], 0, s[12:13]
	s_mov_b32 m0, s30
	s_nop 0
	global_load_lds_dwordx4 v[174:175], off
	s_waitcnt vmcnt(8)
	s_waitcnt lgkmcnt(0)
	s_barrier
	s_setprio 1
	s_waitcnt lgkmcnt(0)
	v_mfma_scale_f32_16x16x128_f8f6f4 v[66:69], v[2:9], v[206:213], v[66:69], v1, v1 op_sel_hi:[0,0,0]
	v_mfma_scale_f32_16x16x128_f8f6f4 v[58:61], v[10:17], v[206:213], v[58:61], v1, v1 op_sel_hi:[0,0,0]
	v_mfma_scale_f32_16x16x128_f8f6f4 v[90:93], v[10:17], v[190:197], v[90:93], v1, v1 op_sel_hi:[0,0,0]
	v_mfma_scale_f32_16x16x128_f8f6f4 v[94:97], v[2:9], v[190:197], v[94:97], v1, v1 op_sel_hi:[0,0,0]
	v_mfma_scale_f32_16x16x128_f8f6f4 v[82:85], v[2:9], v[198:205], v[82:85], v1, v1 op_sel_hi:[0,0,0]
	v_mfma_scale_f32_16x16x128_f8f6f4 v[74:77], v[10:17], v[198:205], v[74:77], v1, v1 op_sel_hi:[0,0,0]
	v_mfma_scale_f32_16x16x128_f8f6f4 v[42:45], v[10:17], v[214:221], v[42:45], v1, v1 op_sel_hi:[0,0,0]
	v_mfma_scale_f32_16x16x128_f8f6f4 v[50:53], v[2:9], v[214:221], v[50:53], v1, v1 op_sel_hi:[0,0,0]
	s_setprio 0
	s_setprio 1
	v_mfma_scale_f32_16x16x128_f8f6f4 v[38:41], v[18:25], v[214:221], v[38:41], v1, v1 op_sel_hi:[0,0,0]
	v_mfma_scale_f32_16x16x128_f8f6f4 v[34:37], v[26:33], v[214:221], v[34:37], v1, v1 op_sel_hi:[0,0,0]
	v_mfma_scale_f32_16x16x128_f8f6f4 v[78:81], v[26:33], v[190:197], v[78:81], v1, v1 op_sel_hi:[0,0,0]
	v_mfma_scale_f32_16x16x128_f8f6f4 v[86:89], v[18:25], v[190:197], v[86:89], v1, v1 op_sel_hi:[0,0,0]
	v_mfma_scale_f32_16x16x128_f8f6f4 v[70:73], v[18:25], v[198:205], v[70:73], v1, v1 op_sel_hi:[0,0,0]
	v_mfma_scale_f32_16x16x128_f8f6f4 v[62:65], v[26:33], v[198:205], v[62:65], v1, v1 op_sel_hi:[0,0,0]
	v_mfma_scale_f32_16x16x128_f8f6f4 v[46:49], v[26:33], v[206:213], v[46:49], v1, v1 op_sel_hi:[0,0,0]
	v_mfma_scale_f32_16x16x128_f8f6f4 v[54:57], v[18:25], v[206:213], v[54:57], v1, v1 op_sel_hi:[0,0,0]
	s_setprio 0
	s_barrier
	s_add_i32 s35, s35, 2
	s_add_u32 s16, s16, 0x100
	s_addc_u32 s17, s17, 0
	s_cmp_gt_u32 s35, 13
	s_cbranch_scc0 .LBB0_1291
	s_cmpk_lt_u32 s19, 0x100
	s_cbranch_scc0 .LBB0_1294
	s_barrier

.LBB0_1309:
	ds_read_b128 v[26:29], v189
	ds_read_b128 v[30:33], v189 offset:1024
	ds_read_b128 v[18:21], v189 offset:2048
	ds_read_b128 v[22:25], v189 offset:3072
	ds_read_b128 v[10:13], v190
	ds_read_b128 v[14:17], v190 offset:1024
	ds_read_b128 v[2:5], v190 offset:2048
	ds_read_b128 v[6:9], v190 offset:3072
	s_add_u32 s40, s38, 0xfff80080
	s_addc_u32 s41, s39, -1
	s_cmp_eq_u32 s72, 28
	s_cselect_b32 s43, s18, s41
	s_cselect_b32 s42, s19, s40
	s_cselect_b32 s41, s27, s71
	s_cselect_b32 s40, s29, s70
	v_lshl_add_u64 v[216:217], s[38:39], 0, v[170:171]
	s_add_i32 m0, s37, 0xc000
	ds_read_b128 v[178:181], v191
	ds_read_b128 v[182:185], v191 offset:1024
	ds_read_b128 v[192:195], v191 offset:2048
	ds_read_b128 v[196:199], v191 offset:3072
	ds_read_b128 v[200:203], v191 offset:4096
	ds_read_b128 v[204:207], v191 offset:5120
	ds_read_b128 v[208:211], v191 offset:6144
	ds_read_b128 v[212:215], v191 offset:7168
	global_load_lds_dwordx4 v[216:217], off
	v_lshl_add_u64 v[216:217], s[38:39], 0, v[172:173]
	s_add_i32 m0, s37, 0xe000
	s_nop 0
	global_load_lds_dwordx4 v[216:217], off
	s_waitcnt vmcnt(8)
	s_waitcnt lgkmcnt(0)
	s_barrier
	s_setprio 1
	s_waitcnt lgkmcnt(0)
	v_mfma_scale_f32_16x16x128_f8f6f4 v[158:161], v[26:33], v[178:185], v[158:161], v1, v1 op_sel_hi:[0,0,0]
	v_mfma_scale_f32_16x16x128_f8f6f4 v[154:157], v[18:25], v[178:185], v[154:157], v1, v1 op_sel_hi:[0,0,0]
	v_mfma_scale_f32_16x16x128_f8f6f4 v[138:141], v[18:25], v[192:199], v[138:141], v1, v1 op_sel_hi:[0,0,0]
	v_mfma_scale_f32_16x16x128_f8f6f4 v[146:149], v[26:33], v[192:199], v[146:149], v1, v1 op_sel_hi:[0,0,0]
	v_mfma_scale_f32_16x16x128_f8f6f4 v[130:133], v[26:33], v[200:207], v[130:133], v1, v1 op_sel_hi:[0,0,0]
	v_mfma_scale_f32_16x16x128_f8f6f4 v[122:125], v[18:25], v[200:207], v[122:125], v1, v1 op_sel_hi:[0,0,0]
	v_mfma_scale_f32_16x16x128_f8f6f4 v[106:109], v[18:25], v[208:215], v[106:109], v1, v1 op_sel_hi:[0,0,0]
	v_mfma_scale_f32_16x16x128_f8f6f4 v[114:117], v[26:33], v[208:215], v[114:117], v1, v1 op_sel_hi:[0,0,0]
	s_setprio 0
	s_setprio 1
	v_mfma_scale_f32_16x16x128_f8f6f4 v[102:105], v[10:17], v[208:215], v[102:105], v1, v1 op_sel_hi:[0,0,0]
	v_mfma_scale_f32_16x16x128_f8f6f4 v[98:101], v[2:9], v[208:215], v[98:101], v1, v1 op_sel_hi:[0,0,0]
	v_mfma_scale_f32_16x16x128_f8f6f4 v[142:145], v[2:9], v[178:185], v[142:145], v1, v1 op_sel_hi:[0,0,0]
	v_mfma_scale_f32_16x16x128_f8f6f4 v[150:153], v[10:17], v[178:185], v[150:153], v1, v1 op_sel_hi:[0,0,0]
	v_mfma_scale_f32_16x16x128_f8f6f4 v[134:137], v[10:17], v[192:199], v[134:137], v1, v1 op_sel_hi:[0,0,0]
	v_mfma_scale_f32_16x16x128_f8f6f4 v[126:129], v[2:9], v[192:199], v[126:129], v1, v1 op_sel_hi:[0,0,0]
	v_mfma_scale_f32_16x16x128_f8f6f4 v[110:113], v[2:9], v[200:207], v[110:113], v1, v1 op_sel_hi:[0,0,0]
	v_mfma_scale_f32_16x16x128_f8f6f4 v[118:121], v[10:17], v[200:207], v[118:121], v1, v1 op_sel_hi:[0,0,0]
	s_setprio 0
	s_barrier
	s_add_i32 s64, s59, s3
	v_lshl_add_u64 v[178:179], s[40:41], 0, v[166:167]
	s_mov_b32 m0, s64
	ds_read_b128 v[192:195], v191 offset:16384
	ds_read_b128 v[196:199], v191 offset:17408
	ds_read_b128 v[200:203], v191 offset:18432
	ds_read_b128 v[204:207], v191 offset:19456
	ds_read_b128 v[208:211], v191 offset:20480
	ds_read_b128 v[212:215], v191 offset:21504
	ds_read_b128 v[216:219], v191 offset:22528
	ds_read_b128 v[220:223], v191 offset:23552
	global_load_lds_dwordx4 v[178:179], off
	s_add_i32 m0, s64, 0x2000
	s_add_u32 s64, s40, 0x80000
	v_lshl_add_u64 v[180:181], s[40:41], 0, v[162:163]
	s_addc_u32 s65, s41, 0
	s_add_i32 s73, s62, s3
	global_load_lds_dwordx4 v[180:181], off
	v_lshl_add_u64 v[182:183], s[64:65], 0, v[166:167]
	s_mov_b32 m0, s73
	v_lshl_add_u64 v[184:185], s[42:43], 0, v[164:165]
	global_load_lds_dwordx4 v[182:183], off
	v_lshl_add_u64 v[182:183], s[64:65], 0, v[162:163]
	s_add_i32 m0, s73, 0x2000
	s_nop 0
	global_load_lds_dwordx4 v[182:183], off
	v_lshl_add_u64 v[182:183], s[42:43], 0, v[168:169]
	s_mov_b32 m0, s37
	s_nop 0
	global_load_lds_dwordx4 v[182:183], off
	s_mov_b32 m0, s44
	s_nop 0
	global_load_lds_dwordx4 v[184:185], off
	s_waitcnt vmcnt(8)
	s_waitcnt lgkmcnt(0)
	s_barrier
	s_setprio 1
	s_waitcnt lgkmcnt(0)
	v_mfma_scale_f32_16x16x128_f8f6f4 v[82:85], v[26:33], v[200:207], v[82:85], v1, v1 op_sel_hi:[0,0,0]
	v_mfma_scale_f32_16x16x128_f8f6f4 v[74:77], v[18:25], v[200:207], v[74:77], v1, v1 op_sel_hi:[0,0,0]
	v_mfma_scale_f32_16x16x128_f8f6f4 v[90:93], v[18:25], v[192:199], v[90:93], v1, v1 op_sel_hi:[0,0,0]
	v_mfma_scale_f32_16x16x128_f8f6f4 v[94:97], v[26:33], v[192:199], v[94:97], v1, v1 op_sel_hi:[0,0,0]
	v_mfma_scale_f32_16x16x128_f8f6f4 v[66:69], v[26:33], v[208:215], v[66:69], v1, v1 op_sel_hi:[0,0,0]
	v_mfma_scale_f32_16x16x128_f8f6f4 v[58:61], v[18:25], v[208:215], v[58:61], v1, v1 op_sel_hi:[0,0,0]
	v_mfma_scale_f32_16x16x128_f8f6f4 v[42:45], v[18:25], v[216:223], v[42:45], v1, v1 op_sel_hi:[0,0,0]
	v_mfma_scale_f32_16x16x128_f8f6f4 v[50:53], v[26:33], v[216:223], v[50:53], v1, v1 op_sel_hi:[0,0,0]
	s_setprio 0
	s_setprio 1
	v_mfma_scale_f32_16x16x128_f8f6f4 v[38:41], v[10:17], v[216:223], v[38:41], v1, v1 op_sel_hi:[0,0,0]
	v_mfma_scale_f32_16x16x128_f8f6f4 v[34:37], v[2:9], v[216:223], v[34:37], v1, v1 op_sel_hi:[0,0,0]
	v_mfma_scale_f32_16x16x128_f8f6f4 v[78:81], v[2:9], v[192:199], v[78:81], v1, v1 op_sel_hi:[0,0,0]
	v_mfma_scale_f32_16x16x128_f8f6f4 v[86:89], v[10:17], v[192:199], v[86:89], v1, v1 op_sel_hi:[0,0,0]
	v_mfma_scale_f32_16x16x128_f8f6f4 v[70:73], v[10:17], v[200:207], v[70:73], v1, v1 op_sel_hi:[0,0,0]
	v_mfma_scale_f32_16x16x128_f8f6f4 v[62:65], v[2:9], v[200:207], v[62:65], v1, v1 op_sel_hi:[0,0,0]
	v_mfma_scale_f32_16x16x128_f8f6f4 v[46:49], v[2:9], v[208:215], v[46:49], v1, v1 op_sel_hi:[0,0,0]
	v_mfma_scale_f32_16x16x128_f8f6f4 v[54:57], v[10:17], v[208:215], v[54:57], v1, v1 op_sel_hi:[0,0,0]
	s_setprio 0
	s_barrier
	s_add_i32 s64, 0, 0x18000
	s_add_i32 s65, 0, 0x1c000
	v_add_u32_e32 v14, s64, v187
	v_add_u32_e32 v30, s65, v187
	ds_read_b128 v[2:5], v14
	ds_read_b128 v[6:9], v14 offset:1024
	ds_read_b128 v[10:13], v14 offset:2048
	ds_read_b128 v[14:17], v14 offset:3072
	ds_read_b128 v[18:21], v30
	ds_read_b128 v[22:25], v30 offset:1024
	ds_read_b128 v[26:29], v30 offset:2048
	ds_read_b128 v[30:33], v30 offset:3072
	s_add_u32 s42, s42, 0x80000
	s_addc_u32 s43, s43, 0
	s_mov_b32 m0, s45
	v_lshl_add_u64 v[224:225], s[42:43], 0, v[168:169]
	ds_read_b128 v[192:195], v191 offset:32768
	ds_read_b128 v[196:199], v191 offset:33792
	ds_read_b128 v[200:203], v191 offset:34816
	ds_read_b128 v[204:207], v191 offset:35840
	ds_read_b128 v[208:211], v191 offset:36864
	ds_read_b128 v[212:215], v191 offset:37888
	ds_read_b128 v[216:219], v191 offset:38912
	ds_read_b128 v[220:223], v191 offset:39936
	global_load_lds_dwordx4 v[224:225], off
	v_lshl_add_u64 v[224:225], s[42:43], 0, v[164:165]
	s_mov_b32 m0, s48
	s_nop 0
	global_load_lds_dwordx4 v[224:225], off
	s_waitcnt vmcnt(8)
	s_waitcnt lgkmcnt(0)
	s_barrier
	s_setprio 1
	s_waitcnt lgkmcnt(0)
	v_mfma_scale_f32_16x16x128_f8f6f4 v[122:125], v[10:17], v[208:215], v[122:125], v1, v1 op_sel_hi:[0,0,0]
	v_mfma_scale_f32_16x16x128_f8f6f4 v[130:133], v[2:9], v[208:215], v[130:133], v1, v1 op_sel_hi:[0,0,0]
	v_mfma_scale_f32_16x16x128_f8f6f4 v[158:161], v[2:9], v[192:199], v[158:161], v1, v1 op_sel_hi:[0,0,0]
	v_mfma_scale_f32_16x16x128_f8f6f4 v[154:157], v[10:17], v[192:199], v[154:157], v1, v1 op_sel_hi:[0,0,0]
	v_mfma_scale_f32_16x16x128_f8f6f4 v[138:141], v[10:17], v[200:207], v[138:141], v1, v1 op_sel_hi:[0,0,0]
	v_mfma_scale_f32_16x16x128_f8f6f4 v[146:149], v[2:9], v[200:207], v[146:149], v1, v1 op_sel_hi:[0,0,0]
	v_mfma_scale_f32_16x16x128_f8f6f4 v[114:117], v[2:9], v[216:223], v[114:117], v1, v1 op_sel_hi:[0,0,0]
	v_mfma_scale_f32_16x16x128_f8f6f4 v[106:109], v[10:17], v[216:223], v[106:109], v1, v1 op_sel_hi:[0,0,0]
	s_setprio 0
	s_setprio 1
	v_mfma_scale_f32_16x16x128_f8f6f4 v[102:105], v[18:25], v[216:223], v[102:105], v1, v1 op_sel_hi:[0,0,0]
	v_mfma_scale_f32_16x16x128_f8f6f4 v[98:101], v[26:33], v[216:223], v[98:101], v1, v1 op_sel_hi:[0,0,0]
	v_mfma_scale_f32_16x16x128_f8f6f4 v[142:145], v[26:33], v[192:199], v[142:145], v1, v1 op_sel_hi:[0,0,0]
	v_mfma_scale_f32_16x16x128_f8f6f4 v[150:153], v[18:25], v[192:199], v[150:153], v1, v1 op_sel_hi:[0,0,0]
	v_mfma_scale_f32_16x16x128_f8f6f4 v[134:137], v[18:25], v[200:207], v[134:137], v1, v1 op_sel_hi:[0,0,0]
	v_mfma_scale_f32_16x16x128_f8f6f4 v[126:129], v[26:33], v[200:207], v[126:129], v1, v1 op_sel_hi:[0,0,0]
	v_mfma_scale_f32_16x16x128_f8f6f4 v[110:113], v[26:33], v[208:215], v[110:113], v1, v1 op_sel_hi:[0,0,0]
	v_mfma_scale_f32_16x16x128_f8f6f4 v[118:121], v[18:25], v[208:215], v[118:121], v1, v1 op_sel_hi:[0,0,0]
	s_setprio 0
	s_barrier
	s_add_i32 s42, s64, s3
	v_lshl_add_u64 v[178:179], v[178:179], 0, s[12:13]
	s_mov_b32 m0, s42
	ds_read_b128 v[192:195], v191 offset:49152
	ds_read_b128 v[196:199], v191 offset:50176
	ds_read_b128 v[200:203], v191 offset:51200
	ds_read_b128 v[204:207], v191 offset:52224
	ds_read_b128 v[208:211], v191 offset:53248
	ds_read_b128 v[212:215], v191 offset:54272
	ds_read_b128 v[216:219], v191 offset:55296
	ds_read_b128 v[220:223], v191 offset:56320
	global_load_lds_dwordx4 v[178:179], off
	s_add_i32 m0, s42, 0x2000
	s_add_u32 s40, s40, 0x80080
	v_lshl_add_u64 v[178:179], v[180:181], 0, s[12:13]
	s_addc_u32 s41, s41, 0
	s_add_i32 s42, s65, s3
	global_load_lds_dwordx4 v[178:179], off
	v_lshl_add_u64 v[178:179], s[40:41], 0, v[166:167]
	s_mov_b32 m0, s42
	s_nop 0
	global_load_lds_dwordx4 v[178:179], off
	v_lshl_add_u64 v[178:179], s[40:41], 0, v[162:163]
	s_add_i32 m0, s42, 0x2000
	s_nop 0
	global_load_lds_dwordx4 v[178:179], off
	v_lshl_add_u64 v[178:179], v[182:183], 0, s[12:13]
	s_mov_b32 m0, s51
	s_nop 0
	global_load_lds_dwordx4 v[178:179], off
	v_lshl_add_u64 v[178:179], v[184:185], 0, s[12:13]
	s_mov_b32 m0, s58
	s_nop 0
	global_load_lds_dwordx4 v[178:179], off
	s_waitcnt vmcnt(8)
	s_waitcnt lgkmcnt(0)
	s_barrier
	s_setprio 1
	s_waitcnt lgkmcnt(0)
	v_mfma_scale_f32_16x16x128_f8f6f4 v[66:69], v[2:9], v[208:215], v[66:69], v1, v1 op_sel_hi:[0,0,0]
	v_mfma_scale_f32_16x16x128_f8f6f4 v[58:61], v[10:17], v[208:215], v[58:61], v1, v1 op_sel_hi:[0,0,0]
	v_mfma_scale_f32_16x16x128_f8f6f4 v[90:93], v[10:17], v[192:199], v[90:93], v1, v1 op_sel_hi:[0,0,0]
	v_mfma_scale_f32_16x16x128_f8f6f4 v[94:97], v[2:9], v[192:199], v[94:97], v1, v1 op_sel_hi:[0,0,0]
	v_mfma_scale_f32_16x16x128_f8f6f4 v[82:85], v[2:9], v[200:207], v[82:85], v1, v1 op_sel_hi:[0,0,0]
	v_mfma_scale_f32_16x16x128_f8f6f4 v[74:77], v[10:17], v[200:207], v[74:77], v1, v1 op_sel_hi:[0,0,0]
	v_mfma_scale_f32_16x16x128_f8f6f4 v[42:45], v[10:17], v[216:223], v[42:45], v1, v1 op_sel_hi:[0,0,0]
	v_mfma_scale_f32_16x16x128_f8f6f4 v[50:53], v[2:9], v[216:223], v[50:53], v1, v1 op_sel_hi:[0,0,0]
	s_setprio 0
	s_setprio 1
	v_mfma_scale_f32_16x16x128_f8f6f4 v[38:41], v[18:25], v[216:223], v[38:41], v1, v1 op_sel_hi:[0,0,0]
	v_mfma_scale_f32_16x16x128_f8f6f4 v[34:37], v[26:33], v[216:223], v[34:37], v1, v1 op_sel_hi:[0,0,0]
	v_mfma_scale_f32_16x16x128_f8f6f4 v[78:81], v[26:33], v[192:199], v[78:81], v1, v1 op_sel_hi:[0,0,0]
	v_mfma_scale_f32_16x16x128_f8f6f4 v[86:89], v[18:25], v[192:199], v[86:89], v1, v1 op_sel_hi:[0,0,0]
	v_mfma_scale_f32_16x16x128_f8f6f4 v[70:73], v[18:25], v[200:207], v[70:73], v1, v1 op_sel_hi:[0,0,0]
	v_mfma_scale_f32_16x16x128_f8f6f4 v[62:65], v[26:33], v[200:207], v[62:65], v1, v1 op_sel_hi:[0,0,0]
	v_mfma_scale_f32_16x16x128_f8f6f4 v[46:49], v[26:33], v[208:215], v[46:49], v1, v1 op_sel_hi:[0,0,0]
	v_mfma_scale_f32_16x16x128_f8f6f4 v[54:57], v[18:25], v[208:215], v[54:57], v1, v1 op_sel_hi:[0,0,0]
	s_setprio 0
	s_barrier
	s_add_i32 s72, s72, 2
	s_add_u32 s38, s38, 0x100
	s_addc_u32 s39, s39, 0
	s_add_u32 s70, s70, 0x100
	s_addc_u32 s71, s71, 0
	s_cmp_gt_u32 s72, 29
	s_cbranch_scc0 .LBB0_1309
	s_and_b64 vcc, exec, s[14:15]
	s_cbranch_vccz .LBB0_1312
	s_barrier

.LBB0_1437:
	v_and_b32_e32 v188, 15, v189
	v_and_b32_e32 v2, 48, v189
	v_lshlrev_b32_e32 v3, 2, v189
	s_and_b32 s8, s6, 3
	s_lshl_b32 s9, s7, 13
	v_lshl_or_b32 v2, v188, 6, v2
	v_and_b32_e32 v3, 32, v3
	v_bitop3_b32 v4, v2, s9, v3 bitop3:0xde
	s_lshl_b32 s9, s8, 12
	v_lshl_add_u64 v[180:181], s[20:21], 0, v[154:155]
	v_bitop3_b32 v2, v2, s9, v3 bitop3:0xde
	s_add_i32 s9, s60, s72
	v_lshl_add_u64 v[178:179], s[20:21], 0, v[182:183]
	v_lshl_add_u64 v[72:73], v[180:181], 0, s[36:37]
	s_mov_b32 m0, s9
	s_add_i32 s19, s9, 0x2000
	s_waitcnt vmcnt(2)
	s_barrier
	global_load_lds_dwordx4 v[72:73], off
	v_lshl_add_u64 v[158:159], v[178:179], 0, s[36:37]
	s_mov_b32 m0, s19
	s_add_i32 s18, s67, 0x8000
	global_load_lds_dwordx4 v[158:159], off
	v_lshl_add_u64 v[70:71], v[172:173], 0, s[36:37]
	s_mov_b32 m0, s18
	s_add_i32 s43, s67, 0xa000
	global_load_lds_dwordx4 v[70:71], off
	v_lshl_add_u64 v[160:161], v[170:171], 0, s[36:37]
	s_mov_b32 m0, s43
	s_add_i32 s44, s61, s72
	global_load_lds_dwordx4 v[160:161], off
	v_lshl_add_u64 v[162:163], s[24:25], 0, v[154:155]
	s_mov_b32 m0, s44
	s_add_i32 s45, s44, 0x2000
	global_load_lds_dwordx4 v[162:163], off
	v_lshl_add_u64 v[164:165], s[24:25], 0, v[182:183]
	s_mov_b32 m0, s45
	s_add_i32 s73, 0, 0x10000
	global_load_lds_dwordx4 v[164:165], off
	v_add_u32_e32 v195, s73, v2
	s_add_i32 s75, 0, 0x14000
	s_waitcnt vmcnt(6)
	s_barrier
	v_add_u32_e32 v194, s75, v2
	v_add_u32_e32 v191, 0, v4
	v_add_u32_e32 v193, s60, v2
	v_add_u32_e32 v192, s61, v2
	ds_read_b128 v[54:57], v195
	ds_read_b128 v[58:61], v195 offset:1024
	ds_read_b128 v[196:199], v195 offset:2048
	ds_read_b128 v[200:203], v195 offset:3072
	ds_read_b128 v[10:13], v194
	ds_read_b128 v[14:17], v194 offset:1024
	ds_read_b128 v[2:5], v194 offset:2048
	ds_read_b128 v[6:9], v194 offset:3072
	s_lshl_b32 s66, s7, 6
	v_lshl_add_u64 v[176:177], s[22:23], 0, v[154:155]
	v_lshl_add_u64 v[174:175], s[22:23], 0, v[182:183]
	s_add_u32 s70, s4, 0x10080
	s_addc_u32 s71, s5, 0
	s_add_i32 s74, s67, 0xc000
	v_lshl_add_u64 v[30:31], s[70:71], 0, v[154:155]
	s_mov_b32 m0, s74
	s_add_i32 s69, s67, 0xe000
	ds_read_b128 v[22:25], v191
	ds_read_b128 v[26:29], v191 offset:1024
	ds_read_b128 v[34:37], v191 offset:2048
	ds_read_b128 v[38:41], v191 offset:3072
	ds_read_b128 v[82:85], v191 offset:4096
	ds_read_b128 v[86:89], v191 offset:5120
	ds_read_b128 v[94:97], v191 offset:6144
	ds_read_b128 v[98:101], v191 offset:7168
	global_load_lds_dwordx4 v[30:31], off
	v_lshl_add_u64 v[30:31], s[70:71], 0, v[182:183]
	s_mov_b32 m0, s69
	s_nop 0
	global_load_lds_dwordx4 v[30:31], off
	s_waitcnt vmcnt(8)
	s_waitcnt lgkmcnt(0)
	s_barrier
	s_setprio 1
	v_mov_b64_e32 v[32:33], v[20:21]
	v_mov_b64_e32 v[152:153], v[20:21]
	v_mov_b64_e32 v[92:93], v[20:21]
	v_mov_b64_e32 v[44:45], v[20:21]
	v_mov_b64_e32 v[116:117], v[20:21]
	v_mov_b64_e32 v[64:65], v[20:21]
	v_mov_b64_e32 v[80:81], v[20:21]
	v_mov_b64_e32 v[52:53], v[20:21]
	v_mov_b64_e32 v[30:31], v[18:19]
	v_mov_b64_e32 v[150:151], v[18:19]
	v_mov_b64_e32 v[90:91], v[18:19]
	v_mov_b64_e32 v[42:43], v[18:19]
	v_mov_b64_e32 v[114:115], v[18:19]
	v_mov_b64_e32 v[62:63], v[18:19]
	v_mov_b64_e32 v[78:79], v[18:19]
	v_mov_b64_e32 v[50:51], v[18:19]
	s_waitcnt lgkmcnt(0)
	v_mfma_scale_f32_16x16x128_f8f6f4 v[30:33], v[54:61], v[22:29], v[30:33], v190, v190 op_sel_hi:[0,0,0]
	v_mfma_scale_f32_16x16x128_f8f6f4 v[150:153], v[196:203], v[22:29], v[150:153], v190, v190 op_sel_hi:[0,0,0]
	v_mfma_scale_f32_16x16x128_f8f6f4 v[42:45], v[196:203], v[34:41], v[42:45], v190, v190 op_sel_hi:[0,0,0]
	v_mfma_scale_f32_16x16x128_f8f6f4 v[90:93], v[54:61], v[34:41], v[90:93], v190, v190 op_sel_hi:[0,0,0]
	v_mfma_scale_f32_16x16x128_f8f6f4 v[114:117], v[54:61], v[82:89], v[114:117], v190, v190 op_sel_hi:[0,0,0]
	v_mfma_scale_f32_16x16x128_f8f6f4 v[62:65], v[196:203], v[82:89], v[62:65], v190, v190 op_sel_hi:[0,0,0]
	v_mfma_scale_f32_16x16x128_f8f6f4 v[50:53], v[196:203], v[94:101], v[50:53], v190, v190 op_sel_hi:[0,0,0]
	v_mfma_scale_f32_16x16x128_f8f6f4 v[78:81], v[54:61], v[94:101], v[78:81], v190, v190 op_sel_hi:[0,0,0]
	s_setprio 0
	s_setprio 1
	v_mov_b64_e32 v[144:145], v[20:21]
	v_mov_b64_e32 v[148:149], v[20:21]
	v_mov_b64_e32 v[142:143], v[18:19]
	v_mov_b64_e32 v[146:147], v[18:19]
	v_mfma_scale_f32_16x16x128_f8f6f4 v[142:145], v[10:17], v[22:29], v[142:145], v190, v190 op_sel_hi:[0,0,0]
	v_mfma_scale_f32_16x16x128_f8f6f4 v[146:149], v[2:9], v[22:29], v[146:149], v190, v190 op_sel_hi:[0,0,0]
	v_mov_b64_e32 v[28:29], v[20:21]
	v_mov_b64_e32 v[140:141], v[20:21]
	v_mov_b64_e32 v[26:27], v[18:19]
	v_mov_b64_e32 v[138:139], v[18:19]
	v_mfma_scale_f32_16x16x128_f8f6f4 v[26:29], v[10:17], v[34:41], v[26:29], v190, v190 op_sel_hi:[0,0,0]
	v_mfma_scale_f32_16x16x128_f8f6f4 v[138:141], v[2:9], v[34:41], v[138:141], v190, v190 op_sel_hi:[0,0,0]
	v_mov_b64_e32 v[40:41], v[20:21]
	v_mov_b64_e32 v[128:129], v[20:21]
	v_mov_b64_e32 v[24:25], v[20:21]
	v_mov_b64_e32 v[76:77], v[20:21]
	v_mov_b64_e32 v[38:39], v[18:19]
	v_mov_b64_e32 v[126:127], v[18:19]
	v_mov_b64_e32 v[22:23], v[18:19]
	v_mov_b64_e32 v[74:75], v[18:19]
	v_mfma_scale_f32_16x16x128_f8f6f4 v[38:41], v[10:17], v[82:89], v[38:41], v190, v190 op_sel_hi:[0,0,0]
	v_mfma_scale_f32_16x16x128_f8f6f4 v[126:129], v[2:9], v[82:89], v[126:129], v190, v190 op_sel_hi:[0,0,0]
	v_mfma_scale_f32_16x16x128_f8f6f4 v[22:25], v[10:17], v[94:101], v[22:25], v190, v190 op_sel_hi:[0,0,0]
	v_mfma_scale_f32_16x16x128_f8f6f4 v[74:77], v[2:9], v[94:101], v[74:77], v190, v190 op_sel_hi:[0,0,0]
	s_setprio 0
	s_barrier
	s_add_i32 s70, s73, s72
	v_lshl_add_u64 v[34:35], v[180:181], 0, s[14:15]
	s_mov_b32 m0, s70
	s_add_i32 s71, s70, 0x2000
	ds_read_b128 v[204:207], v191 offset:16384
	ds_read_b128 v[208:211], v191 offset:17408
	ds_read_b128 v[212:215], v191 offset:18432
	ds_read_b128 v[216:219], v191 offset:19456
	ds_read_b128 v[220:223], v191 offset:20480
	ds_read_b128 v[224:227], v191 offset:21504
	ds_read_b128 v[228:231], v191 offset:22528
	ds_read_b128 v[232:235], v191 offset:23552
	global_load_lds_dwordx4 v[34:35], off
	v_lshl_add_u64 v[34:35], v[178:179], 0, s[14:15]
	s_mov_b32 m0, s71
	s_add_i32 s72, s75, s72
	global_load_lds_dwordx4 v[34:35], off
	v_lshl_add_u64 v[34:35], s[26:27], 0, v[154:155]
	s_mov_b32 m0, s72
	s_add_i32 s73, s72, 0x2000
	global_load_lds_dwordx4 v[34:35], off
	v_lshl_add_u64 v[34:35], s[26:27], 0, v[182:183]
	s_mov_b32 m0, s73
	s_nop 0
	global_load_lds_dwordx4 v[34:35], off
	v_lshl_add_u64 v[34:35], v[172:173], 0, s[14:15]
	s_mov_b32 m0, s67
	s_nop 0
	global_load_lds_dwordx4 v[34:35], off
	v_lshl_add_u64 v[34:35], v[170:171], 0, s[14:15]
	s_mov_b32 m0, s68
	s_nop 0
	global_load_lds_dwordx4 v[34:35], off
	s_waitcnt vmcnt(8)
	s_waitcnt lgkmcnt(0)
	s_barrier
	s_setprio 1
	v_mov_b64_e32 v[136:137], v[20:21]
	v_mov_b64_e32 v[104:105], v[20:21]
	v_mov_b64_e32 v[124:125], v[20:21]
	v_mov_b64_e32 v[100:101], v[20:21]
	v_mov_b64_e32 v[112:113], v[20:21]
	v_mov_b64_e32 v[108:109], v[20:21]
	v_mov_b64_e32 v[88:89], v[20:21]
	v_mov_b64_e32 v[84:85], v[20:21]
	v_mov_b64_e32 v[134:135], v[18:19]
	v_mov_b64_e32 v[102:103], v[18:19]
	v_mov_b64_e32 v[122:123], v[18:19]
	v_mov_b64_e32 v[98:99], v[18:19]
	v_mov_b64_e32 v[110:111], v[18:19]
	v_mov_b64_e32 v[106:107], v[18:19]
	v_mov_b64_e32 v[86:87], v[18:19]
	v_mov_b64_e32 v[82:83], v[18:19]
	s_waitcnt lgkmcnt(0)
	v_mfma_scale_f32_16x16x128_f8f6f4 v[134:137], v[54:61], v[204:211], v[134:137], v190, v190 op_sel_hi:[0,0,0]
	v_mfma_scale_f32_16x16x128_f8f6f4 v[102:105], v[196:203], v[204:211], v[102:105], v190, v190 op_sel_hi:[0,0,0]
	v_mfma_scale_f32_16x16x128_f8f6f4 v[98:101], v[196:203], v[212:219], v[98:101], v190, v190 op_sel_hi:[0,0,0]
	v_mfma_scale_f32_16x16x128_f8f6f4 v[122:125], v[54:61], v[212:219], v[122:125], v190, v190 op_sel_hi:[0,0,0]
	v_mfma_scale_f32_16x16x128_f8f6f4 v[110:113], v[54:61], v[220:227], v[110:113], v190, v190 op_sel_hi:[0,0,0]
	v_mfma_scale_f32_16x16x128_f8f6f4 v[106:109], v[196:203], v[220:227], v[106:109], v190, v190 op_sel_hi:[0,0,0]
	v_mfma_scale_f32_16x16x128_f8f6f4 v[82:85], v[196:203], v[228:235], v[82:85], v190, v190 op_sel_hi:[0,0,0]
	v_mfma_scale_f32_16x16x128_f8f6f4 v[86:89], v[54:61], v[228:235], v[86:89], v190, v190 op_sel_hi:[0,0,0]
	s_setprio 0
	s_setprio 1
	v_mov_b64_e32 v[36:37], v[20:21]
	v_mov_b64_e32 v[132:133], v[20:21]
	v_mov_b64_e32 v[48:49], v[20:21]
	v_mov_b64_e32 v[120:121], v[20:21]
	v_mov_b64_e32 v[68:69], v[20:21]
	v_mov_b64_e32 v[96:97], v[20:21]
	v_mov_b64_e32 v[56:57], v[20:21]
	v_mov_b64_e32 v[60:61], v[20:21]
	v_mov_b64_e32 v[34:35], v[18:19]
	v_mov_b64_e32 v[130:131], v[18:19]
	v_mov_b64_e32 v[46:47], v[18:19]
	v_mov_b64_e32 v[118:119], v[18:19]
	v_mov_b64_e32 v[66:67], v[18:19]
	v_mov_b64_e32 v[94:95], v[18:19]
	v_mov_b64_e32 v[54:55], v[18:19]
	v_mov_b64_e32 v[58:59], v[18:19]
	v_mfma_scale_f32_16x16x128_f8f6f4 v[54:57], v[10:17], v[228:235], v[54:57], v190, v190 op_sel_hi:[0,0,0]
	v_mfma_scale_f32_16x16x128_f8f6f4 v[58:61], v[2:9], v[228:235], v[58:61], v190, v190 op_sel_hi:[0,0,0]
	v_mfma_scale_f32_16x16x128_f8f6f4 v[130:133], v[2:9], v[204:211], v[130:133], v190, v190 op_sel_hi:[0,0,0]
	v_mfma_scale_f32_16x16x128_f8f6f4 v[34:37], v[10:17], v[204:211], v[34:37], v190, v190 op_sel_hi:[0,0,0]
	v_mfma_scale_f32_16x16x128_f8f6f4 v[46:49], v[10:17], v[212:219], v[46:49], v190, v190 op_sel_hi:[0,0,0]
	v_mfma_scale_f32_16x16x128_f8f6f4 v[118:121], v[2:9], v[212:219], v[118:121], v190, v190 op_sel_hi:[0,0,0]
	v_mfma_scale_f32_16x16x128_f8f6f4 v[94:97], v[2:9], v[220:227], v[94:97], v190, v190 op_sel_hi:[0,0,0]
	v_mfma_scale_f32_16x16x128_f8f6f4 v[66:69], v[10:17], v[220:227], v[66:69], v190, v190 op_sel_hi:[0,0,0]
	s_setprio 0
	s_barrier
	ds_read_b128 v[2:5], v193
	ds_read_b128 v[6:9], v193 offset:1024
	ds_read_b128 v[10:13], v193 offset:2048
	ds_read_b128 v[14:17], v193 offset:3072
	ds_read_b128 v[196:199], v192
	ds_read_b128 v[200:203], v192 offset:1024
	ds_read_b128 v[204:207], v192 offset:2048
	ds_read_b128 v[208:211], v192 offset:3072
	s_add_u32 s76, s4, 0x10100
	s_addc_u32 s77, s5, 0
	s_mov_b32 m0, s48
	v_lshl_add_u64 v[244:245], s[76:77], 0, v[154:155]
	ds_read_b128 v[212:215], v191 offset:32768
	ds_read_b128 v[216:219], v191 offset:33792
	ds_read_b128 v[220:223], v191 offset:34816
	ds_read_b128 v[224:227], v191 offset:35840
	ds_read_b128 v[228:231], v191 offset:36864
	ds_read_b128 v[232:235], v191 offset:37888
	ds_read_b128 v[236:239], v191 offset:38912
	ds_read_b128 v[240:243], v191 offset:39936
	global_load_lds_dwordx4 v[244:245], off
	v_lshl_add_u64 v[244:245], s[76:77], 0, v[182:183]
	s_mov_b32 m0, s49
	s_nop 0
	global_load_lds_dwordx4 v[244:245], off
	s_waitcnt vmcnt(8)
	s_waitcnt lgkmcnt(0)
	s_barrier
	s_setprio 1
	s_waitcnt lgkmcnt(0)
	v_mfma_scale_f32_16x16x128_f8f6f4 v[42:45], v[10:17], v[220:227], v[42:45], v190, v190 op_sel_hi:[0,0,0]
	v_mfma_scale_f32_16x16x128_f8f6f4 v[90:93], v[2:9], v[220:227], v[90:93], v190, v190 op_sel_hi:[0,0,0]
	v_mfma_scale_f32_16x16x128_f8f6f4 v[30:33], v[2:9], v[212:219], v[30:33], v190, v190 op_sel_hi:[0,0,0]
	v_mfma_scale_f32_16x16x128_f8f6f4 v[150:153], v[10:17], v[212:219], v[150:153], v190, v190 op_sel_hi:[0,0,0]
	v_mfma_scale_f32_16x16x128_f8f6f4 v[62:65], v[10:17], v[228:235], v[62:65], v190, v190 op_sel_hi:[0,0,0]
	v_mfma_scale_f32_16x16x128_f8f6f4 v[114:117], v[2:9], v[228:235], v[114:117], v190, v190 op_sel_hi:[0,0,0]
	v_mfma_scale_f32_16x16x128_f8f6f4 v[78:81], v[2:9], v[236:243], v[78:81], v190, v190 op_sel_hi:[0,0,0]
	v_mfma_scale_f32_16x16x128_f8f6f4 v[50:53], v[10:17], v[236:243], v[50:53], v190, v190 op_sel_hi:[0,0,0]
	s_setprio 0
	s_setprio 1
	v_mfma_scale_f32_16x16x128_f8f6f4 v[22:25], v[196:203], v[236:243], v[22:25], v190, v190 op_sel_hi:[0,0,0]
	v_mfma_scale_f32_16x16x128_f8f6f4 v[74:77], v[204:211], v[236:243], v[74:77], v190, v190 op_sel_hi:[0,0,0]
	v_mfma_scale_f32_16x16x128_f8f6f4 v[146:149], v[204:211], v[212:219], v[146:149], v190, v190 op_sel_hi:[0,0,0]
	v_mfma_scale_f32_16x16x128_f8f6f4 v[142:145], v[196:203], v[212:219], v[142:145], v190, v190 op_sel_hi:[0,0,0]
	v_mfma_scale_f32_16x16x128_f8f6f4 v[26:29], v[196:203], v[220:227], v[26:29], v190, v190 op_sel_hi:[0,0,0]
	v_mfma_scale_f32_16x16x128_f8f6f4 v[138:141], v[204:211], v[220:227], v[138:141], v190, v190 op_sel_hi:[0,0,0]
	v_mfma_scale_f32_16x16x128_f8f6f4 v[126:129], v[204:211], v[228:235], v[126:129], v190, v190 op_sel_hi:[0,0,0]
	v_mfma_scale_f32_16x16x128_f8f6f4 v[38:41], v[196:203], v[228:235], v[38:41], v190, v190 op_sel_hi:[0,0,0]
	s_setprio 0
	s_barrier
	s_mov_b32 m0, s9
	v_lshl_add_u64 v[244:245], v[180:181], 0, s[38:39]
	ds_read_b128 v[212:215], v191 offset:49152
	ds_read_b128 v[216:219], v191 offset:50176
	ds_read_b128 v[220:223], v191 offset:51200
	ds_read_b128 v[224:227], v191 offset:52224
	ds_read_b128 v[228:231], v191 offset:53248
	ds_read_b128 v[232:235], v191 offset:54272
	ds_read_b128 v[236:239], v191 offset:55296
	ds_read_b128 v[240:243], v191 offset:56320
	global_load_lds_dwordx4 v[244:245], off
	v_lshl_add_u64 v[244:245], v[178:179], 0, s[38:39]
	s_mov_b32 m0, s19
	s_nop 0
	global_load_lds_dwordx4 v[244:245], off
	v_lshl_add_u64 v[244:245], s[28:29], 0, v[154:155]
	s_mov_b32 m0, s44
	s_nop 0
	global_load_lds_dwordx4 v[244:245], off
	v_lshl_add_u64 v[244:245], s[28:29], 0, v[182:183]
	s_mov_b32 m0, s45
	s_nop 0
	global_load_lds_dwordx4 v[244:245], off
	v_lshl_add_u64 v[244:245], v[172:173], 0, s[38:39]
	s_mov_b32 m0, s18
	s_nop 0
	global_load_lds_dwordx4 v[244:245], off
	v_lshl_add_u64 v[244:245], v[170:171], 0, s[38:39]
	s_mov_b32 m0, s43
	s_nop 0
	global_load_lds_dwordx4 v[244:245], off
	s_waitcnt vmcnt(8)
	s_waitcnt lgkmcnt(0)
	s_barrier
	s_setprio 1
	s_waitcnt lgkmcnt(0)
	v_mfma_scale_f32_16x16x128_f8f6f4 v[110:113], v[2:9], v[228:235], v[110:113], v190, v190 op_sel_hi:[0,0,0]
	v_mfma_scale_f32_16x16x128_f8f6f4 v[106:109], v[10:17], v[228:235], v[106:109], v190, v190 op_sel_hi:[0,0,0]
	v_mfma_scale_f32_16x16x128_f8f6f4 v[102:105], v[10:17], v[212:219], v[102:105], v190, v190 op_sel_hi:[0,0,0]
	v_mfma_scale_f32_16x16x128_f8f6f4 v[134:137], v[2:9], v[212:219], v[134:137], v190, v190 op_sel_hi:[0,0,0]
	v_mfma_scale_f32_16x16x128_f8f6f4 v[122:125], v[2:9], v[220:227], v[122:125], v190, v190 op_sel_hi:[0,0,0]
	v_mfma_scale_f32_16x16x128_f8f6f4 v[98:101], v[10:17], v[220:227], v[98:101], v190, v190 op_sel_hi:[0,0,0]
	v_mfma_scale_f32_16x16x128_f8f6f4 v[82:85], v[10:17], v[236:243], v[82:85], v190, v190 op_sel_hi:[0,0,0]
	v_mfma_scale_f32_16x16x128_f8f6f4 v[86:89], v[2:9], v[236:243], v[86:89], v190, v190 op_sel_hi:[0,0,0]
	s_setprio 0
	s_setprio 1
	v_mfma_scale_f32_16x16x128_f8f6f4 v[54:57], v[196:203], v[236:243], v[54:57], v190, v190 op_sel_hi:[0,0,0]
	v_mfma_scale_f32_16x16x128_f8f6f4 v[58:61], v[204:211], v[236:243], v[58:61], v190, v190 op_sel_hi:[0,0,0]
	v_mfma_scale_f32_16x16x128_f8f6f4 v[130:133], v[204:211], v[212:219], v[130:133], v190, v190 op_sel_hi:[0,0,0]
	v_mfma_scale_f32_16x16x128_f8f6f4 v[34:37], v[196:203], v[212:219], v[34:37], v190, v190 op_sel_hi:[0,0,0]
	v_mfma_scale_f32_16x16x128_f8f6f4 v[46:49], v[196:203], v[220:227], v[46:49], v190, v190 op_sel_hi:[0,0,0]
	v_mfma_scale_f32_16x16x128_f8f6f4 v[118:121], v[204:211], v[220:227], v[118:121], v190, v190 op_sel_hi:[0,0,0]
	v_mfma_scale_f32_16x16x128_f8f6f4 v[94:97], v[204:211], v[228:235], v[94:97], v190, v190 op_sel_hi:[0,0,0]
	v_mfma_scale_f32_16x16x128_f8f6f4 v[66:69], v[196:203], v[228:235], v[66:69], v190, v190 op_sel_hi:[0,0,0]
	s_setprio 0
	s_barrier
	ds_read_b128 v[2:5], v195
	ds_read_b128 v[6:9], v195 offset:1024
	ds_read_b128 v[10:13], v195 offset:2048
	ds_read_b128 v[14:17], v195 offset:3072
	ds_read_b128 v[196:199], v194
	ds_read_b128 v[200:203], v194 offset:1024
	ds_read_b128 v[204:207], v194 offset:2048
	ds_read_b128 v[208:211], v194 offset:3072
	s_add_u32 s4, s4, 0x10180
	s_addc_u32 s5, s5, 0
	s_mov_b32 m0, s74
	v_lshl_add_u64 v[194:195], s[4:5], 0, v[154:155]
	ds_read_b128 v[212:215], v191
	ds_read_b128 v[216:219], v191 offset:1024
	ds_read_b128 v[220:223], v191 offset:2048
	ds_read_b128 v[224:227], v191 offset:3072
	ds_read_b128 v[228:231], v191 offset:4096
	ds_read_b128 v[232:235], v191 offset:5120
	ds_read_b128 v[236:239], v191 offset:6144
	ds_read_b128 v[240:243], v191 offset:7168
	global_load_lds_dwordx4 v[194:195], off
	v_lshl_add_u64 v[182:183], s[4:5], 0, v[182:183]
	s_mov_b32 m0, s69
	s_nop 0
	global_load_lds_dwordx4 v[182:183], off
	s_waitcnt vmcnt(8)
	s_waitcnt lgkmcnt(0)
	s_barrier
	s_setprio 1
	s_waitcnt lgkmcnt(0)
	v_mfma_scale_f32_16x16x128_f8f6f4 v[114:117], v[2:9], v[228:235], v[114:117], v190, v190 op_sel_hi:[0,0,0]
	v_mfma_scale_f32_16x16x128_f8f6f4 v[62:65], v[10:17], v[228:235], v[62:65], v190, v190 op_sel_hi:[0,0,0]
	v_mfma_scale_f32_16x16x128_f8f6f4 v[150:153], v[10:17], v[212:219], v[150:153], v190, v190 op_sel_hi:[0,0,0]
	v_mfma_scale_f32_16x16x128_f8f6f4 v[30:33], v[2:9], v[212:219], v[30:33], v190, v190 op_sel_hi:[0,0,0]
	v_mfma_scale_f32_16x16x128_f8f6f4 v[90:93], v[2:9], v[220:227], v[90:93], v190, v190 op_sel_hi:[0,0,0]
	v_mfma_scale_f32_16x16x128_f8f6f4 v[42:45], v[10:17], v[220:227], v[42:45], v190, v190 op_sel_hi:[0,0,0]
	v_mfma_scale_f32_16x16x128_f8f6f4 v[50:53], v[10:17], v[236:243], v[50:53], v190, v190 op_sel_hi:[0,0,0]
	v_mfma_scale_f32_16x16x128_f8f6f4 v[78:81], v[2:9], v[236:243], v[78:81], v190, v190 op_sel_hi:[0,0,0]
	s_setprio 0
	s_setprio 1
	v_mfma_scale_f32_16x16x128_f8f6f4 v[22:25], v[196:203], v[236:243], v[22:25], v190, v190 op_sel_hi:[0,0,0]
	v_mfma_scale_f32_16x16x128_f8f6f4 v[74:77], v[204:211], v[236:243], v[74:77], v190, v190 op_sel_hi:[0,0,0]
	v_mfma_scale_f32_16x16x128_f8f6f4 v[146:149], v[204:211], v[212:219], v[146:149], v190, v190 op_sel_hi:[0,0,0]
	v_mfma_scale_f32_16x16x128_f8f6f4 v[142:145], v[196:203], v[212:219], v[142:145], v190, v190 op_sel_hi:[0,0,0]
	v_mfma_scale_f32_16x16x128_f8f6f4 v[26:29], v[196:203], v[220:227], v[26:29], v190, v190 op_sel_hi:[0,0,0]
	v_mfma_scale_f32_16x16x128_f8f6f4 v[138:141], v[204:211], v[220:227], v[138:141], v190, v190 op_sel_hi:[0,0,0]
	v_mfma_scale_f32_16x16x128_f8f6f4 v[126:129], v[204:211], v[228:235], v[126:129], v190, v190 op_sel_hi:[0,0,0]
	v_mfma_scale_f32_16x16x128_f8f6f4 v[38:41], v[196:203], v[228:235], v[38:41], v190, v190 op_sel_hi:[0,0,0]
	s_setprio 0
	s_barrier
	s_mov_b32 m0, s70
	ds_read_b128 v[212:215], v191 offset:16384
	ds_read_b128 v[216:219], v191 offset:17408
	ds_read_b128 v[220:223], v191 offset:18432
	ds_read_b128 v[224:227], v191 offset:19456
	ds_read_b128 v[228:231], v191 offset:20480
	ds_read_b128 v[232:235], v191 offset:21504
	ds_read_b128 v[236:239], v191 offset:22528
	ds_read_b128 v[240:243], v191 offset:23552
	global_load_lds_dwordx4 v[180:181], off
	s_mov_b32 m0, s71
	s_nop 0
	global_load_lds_dwordx4 v[178:179], off
	s_mov_b32 m0, s72
	s_nop 0
	global_load_lds_dwordx4 v[176:177], off
	s_mov_b32 m0, s73
	s_nop 0
	global_load_lds_dwordx4 v[174:175], off
	s_mov_b32 m0, s67
	s_nop 0
	global_load_lds_dwordx4 v[172:173], off
	s_mov_b32 m0, s68
	s_nop 0
	global_load_lds_dwordx4 v[170:171], off
	s_waitcnt vmcnt(8)
	s_waitcnt lgkmcnt(0)
	s_barrier
	s_setprio 1
	s_waitcnt lgkmcnt(0)
	v_mfma_scale_f32_16x16x128_f8f6f4 v[110:113], v[2:9], v[228:235], v[110:113], v190, v190 op_sel_hi:[0,0,0]
	v_mfma_scale_f32_16x16x128_f8f6f4 v[106:109], v[10:17], v[228:235], v[106:109], v190, v190 op_sel_hi:[0,0,0]
	v_mfma_scale_f32_16x16x128_f8f6f4 v[102:105], v[10:17], v[212:219], v[102:105], v190, v190 op_sel_hi:[0,0,0]
	v_mfma_scale_f32_16x16x128_f8f6f4 v[134:137], v[2:9], v[212:219], v[134:137], v190, v190 op_sel_hi:[0,0,0]
	v_mfma_scale_f32_16x16x128_f8f6f4 v[122:125], v[2:9], v[220:227], v[122:125], v190, v190 op_sel_hi:[0,0,0]
	v_mfma_scale_f32_16x16x128_f8f6f4 v[98:101], v[10:17], v[220:227], v[98:101], v190, v190 op_sel_hi:[0,0,0]
	v_mfma_scale_f32_16x16x128_f8f6f4 v[82:85], v[10:17], v[236:243], v[82:85], v190, v190 op_sel_hi:[0,0,0]
	v_mfma_scale_f32_16x16x128_f8f6f4 v[86:89], v[2:9], v[236:243], v[86:89], v190, v190 op_sel_hi:[0,0,0]
	s_setprio 0
	s_setprio 1
	v_mfma_scale_f32_16x16x128_f8f6f4 v[54:57], v[196:203], v[236:243], v[54:57], v190, v190 op_sel_hi:[0,0,0]
	v_mfma_scale_f32_16x16x128_f8f6f4 v[58:61], v[204:211], v[236:243], v[58:61], v190, v190 op_sel_hi:[0,0,0]
	v_mfma_scale_f32_16x16x128_f8f6f4 v[130:133], v[204:211], v[212:219], v[130:133], v190, v190 op_sel_hi:[0,0,0]
	v_mfma_scale_f32_16x16x128_f8f6f4 v[34:37], v[196:203], v[212:219], v[34:37], v190, v190 op_sel_hi:[0,0,0]
	v_mfma_scale_f32_16x16x128_f8f6f4 v[46:49], v[196:203], v[220:227], v[46:49], v190, v190 op_sel_hi:[0,0,0]
	v_mfma_scale_f32_16x16x128_f8f6f4 v[118:121], v[204:211], v[220:227], v[118:121], v190, v190 op_sel_hi:[0,0,0]
	v_mfma_scale_f32_16x16x128_f8f6f4 v[94:97], v[204:211], v[228:235], v[94:97], v190, v190 op_sel_hi:[0,0,0]
	v_mfma_scale_f32_16x16x128_f8f6f4 v[66:69], v[196:203], v[228:235], v[66:69], v190, v190 op_sel_hi:[0,0,0]
	s_setprio 0
	s_barrier
	ds_read_b128 v[2:5], v193
	ds_read_b128 v[6:9], v193 offset:1024
	ds_read_b128 v[10:13], v193 offset:2048
	ds_read_b128 v[14:17], v193 offset:3072
	ds_read_b128 v[170:173], v192
	ds_read_b128 v[174:177], v192 offset:1024
	ds_read_b128 v[194:197], v192 offset:2048
	ds_read_b128 v[198:201], v192 offset:3072
	s_mov_b32 m0, s48
	ds_read_b128 v[202:205], v191 offset:32768
	ds_read_b128 v[206:209], v191 offset:33792
	ds_read_b128 v[210:213], v191 offset:34816
	ds_read_b128 v[214:217], v191 offset:35840
	ds_read_b128 v[218:221], v191 offset:36864
	ds_read_b128 v[222:225], v191 offset:37888
	ds_read_b128 v[226:229], v191 offset:38912
	ds_read_b128 v[230:233], v191 offset:39936
	global_load_lds_dwordx4 v[166:167], off
	s_mov_b32 m0, s49
	s_nop 0
	global_load_lds_dwordx4 v[168:169], off
	s_waitcnt vmcnt(8)
	s_waitcnt lgkmcnt(0)
	s_barrier
	s_setprio 1
	s_waitcnt lgkmcnt(0)
	v_mfma_scale_f32_16x16x128_f8f6f4 v[30:33], v[2:9], v[202:209], v[30:33], v190, v190 op_sel_hi:[0,0,0]
	v_mfma_scale_f32_16x16x128_f8f6f4 v[150:153], v[10:17], v[202:209], v[150:153], v190, v190 op_sel_hi:[0,0,0]
	v_mfma_scale_f32_16x16x128_f8f6f4 v[42:45], v[10:17], v[210:217], v[42:45], v190, v190 op_sel_hi:[0,0,0]
	v_mfma_scale_f32_16x16x128_f8f6f4 v[90:93], v[2:9], v[210:217], v[90:93], v190, v190 op_sel_hi:[0,0,0]
	v_mfma_scale_f32_16x16x128_f8f6f4 v[114:117], v[2:9], v[218:225], v[114:117], v190, v190 op_sel_hi:[0,0,0]
	v_mfma_scale_f32_16x16x128_f8f6f4 v[62:65], v[10:17], v[218:225], v[62:65], v190, v190 op_sel_hi:[0,0,0]
	v_mfma_scale_f32_16x16x128_f8f6f4 v[50:53], v[10:17], v[226:233], v[50:53], v190, v190 op_sel_hi:[0,0,0]
	v_mfma_scale_f32_16x16x128_f8f6f4 v[78:81], v[2:9], v[226:233], v[78:81], v190, v190 op_sel_hi:[0,0,0]
	s_setprio 0
	s_setprio 1
	v_mfma_scale_f32_16x16x128_f8f6f4 v[22:25], v[170:177], v[226:233], v[22:25], v190, v190 op_sel_hi:[0,0,0]
	v_mfma_scale_f32_16x16x128_f8f6f4 v[74:77], v[194:201], v[226:233], v[74:77], v190, v190 op_sel_hi:[0,0,0]
	v_mfma_scale_f32_16x16x128_f8f6f4 v[146:149], v[194:201], v[202:209], v[146:149], v190, v190 op_sel_hi:[0,0,0]
	v_mfma_scale_f32_16x16x128_f8f6f4 v[142:145], v[170:177], v[202:209], v[142:145], v190, v190 op_sel_hi:[0,0,0]
	v_mfma_scale_f32_16x16x128_f8f6f4 v[26:29], v[170:177], v[210:217], v[26:29], v190, v190 op_sel_hi:[0,0,0]
	v_mfma_scale_f32_16x16x128_f8f6f4 v[138:141], v[194:201], v[210:217], v[138:141], v190, v190 op_sel_hi:[0,0,0]
	v_mfma_scale_f32_16x16x128_f8f6f4 v[126:129], v[194:201], v[218:225], v[126:129], v190, v190 op_sel_hi:[0,0,0]
	v_mfma_scale_f32_16x16x128_f8f6f4 v[38:41], v[170:177], v[218:225], v[38:41], v190, v190 op_sel_hi:[0,0,0]
	s_setprio 0
	s_barrier
	s_mov_b32 m0, s9
	ds_read_b128 v[202:205], v191 offset:49152
	ds_read_b128 v[206:209], v191 offset:50176
	ds_read_b128 v[210:213], v191 offset:51200
	ds_read_b128 v[214:217], v191 offset:52224
	ds_read_b128 v[218:221], v191 offset:53248
	ds_read_b128 v[222:225], v191 offset:54272
	ds_read_b128 v[226:229], v191 offset:55296
	ds_read_b128 v[230:233], v191 offset:56320
	global_load_lds_dwordx4 v[72:73], off
	s_mov_b32 m0, s19
	s_nop 0
	global_load_lds_dwordx4 v[158:159], off
	s_mov_b32 m0, s44
	s_nop 0
	global_load_lds_dwordx4 v[162:163], off
	s_mov_b32 m0, s45
	s_nop 0
	global_load_lds_dwordx4 v[164:165], off
	s_mov_b32 m0, s18
	s_nop 0
	global_load_lds_dwordx4 v[70:71], off
	s_mov_b32 m0, s43
	s_nop 0
	global_load_lds_dwordx4 v[160:161], off
	s_waitcnt vmcnt(8)
	s_waitcnt lgkmcnt(0)
	s_barrier
	s_setprio 1
	s_waitcnt lgkmcnt(0)
	v_mfma_scale_f32_16x16x128_f8f6f4 v[110:113], v[2:9], v[218:225], v[110:113], v190, v190 op_sel_hi:[0,0,0]
	v_mfma_scale_f32_16x16x128_f8f6f4 v[106:109], v[10:17], v[218:225], v[106:109], v190, v190 op_sel_hi:[0,0,0]
	v_mfma_scale_f32_16x16x128_f8f6f4 v[102:105], v[10:17], v[202:209], v[102:105], v190, v190 op_sel_hi:[0,0,0]
	v_mfma_scale_f32_16x16x128_f8f6f4 v[134:137], v[2:9], v[202:209], v[134:137], v190, v190 op_sel_hi:[0,0,0]
	v_mfma_scale_f32_16x16x128_f8f6f4 v[122:125], v[2:9], v[210:217], v[122:125], v190, v190 op_sel_hi:[0,0,0]
	v_mfma_scale_f32_16x16x128_f8f6f4 v[98:101], v[10:17], v[210:217], v[98:101], v190, v190 op_sel_hi:[0,0,0]
	v_mfma_scale_f32_16x16x128_f8f6f4 v[82:85], v[10:17], v[226:233], v[82:85], v190, v190 op_sel_hi:[0,0,0]
	v_mfma_scale_f32_16x16x128_f8f6f4 v[86:89], v[2:9], v[226:233], v[86:89], v190, v190 op_sel_hi:[0,0,0]
	s_setprio 0
	s_setprio 1
	v_mfma_scale_f32_16x16x128_f8f6f4 v[54:57], v[170:177], v[226:233], v[54:57], v190, v190 op_sel_hi:[0,0,0]
	v_mfma_scale_f32_16x16x128_f8f6f4 v[58:61], v[194:201], v[226:233], v[58:61], v190, v190 op_sel_hi:[0,0,0]
	v_mfma_scale_f32_16x16x128_f8f6f4 v[130:133], v[194:201], v[202:209], v[130:133], v190, v190 op_sel_hi:[0,0,0]
	v_mfma_scale_f32_16x16x128_f8f6f4 v[34:37], v[170:177], v[202:209], v[34:37], v190, v190 op_sel_hi:[0,0,0]
	v_mfma_scale_f32_16x16x128_f8f6f4 v[46:49], v[170:177], v[210:217], v[46:49], v190, v190 op_sel_hi:[0,0,0]
	v_mfma_scale_f32_16x16x128_f8f6f4 v[118:121], v[194:201], v[210:217], v[118:121], v190, v190 op_sel_hi:[0,0,0]
	v_mfma_scale_f32_16x16x128_f8f6f4 v[94:97], v[194:201], v[218:225], v[94:97], v190, v190 op_sel_hi:[0,0,0]
	v_mfma_scale_f32_16x16x128_f8f6f4 v[66:69], v[170:177], v[218:225], v[66:69], v190, v190 op_sel_hi:[0,0,0]
	s_setprio 0
	s_barrier
	s_waitcnt vmcnt(0)
	s_cmpk_gt_u32 s65, 0xff
	s_cbranch_scc1 .LBB0_1439
	s_barrier

.LBB0_1558:
	s_add_u32 s39, s30, s38
	s_addc_u32 s44, s31, 0
	s_add_u32 s42, s39, 0x100
	s_addc_u32 s43, s44, 0
	s_and_b64 s[40:41], s[36:37], exec
	s_cselect_b32 s41, s18, s43
	s_cselect_b32 s40, s19, s42
	s_add_u32 s38, s28, s38
	s_addc_u32 s42, s29, 0
	s_add_u32 s38, s38, 0x100
	s_addc_u32 s42, s42, 0
	s_and_b64 s[36:37], s[36:37], exec
	s_cselect_b32 s43, s17, s42
	s_cselect_b32 s42, s21, s38
	s_add_u32 s76, s39, 0x10080
	ds_read_b128 v[26:29], v181
	ds_read_b128 v[30:33], v181 offset:1024
	ds_read_b128 v[18:21], v181 offset:2048
	ds_read_b128 v[22:25], v181 offset:3072
	ds_read_b128 v[10:13], v182
	ds_read_b128 v[14:17], v182 offset:1024
	ds_read_b128 v[2:5], v182 offset:2048
	ds_read_b128 v[6:9], v182 offset:3072
	s_addc_u32 s77, s44, 0
	s_add_i32 s75, s63, s15
	s_add_i32 m0, s27, 0xc000
	s_add_i32 s78, s27, 0xe000
	s_add_i32 s72, s75, 0x2000
	s_add_u32 s44, s42, 0x10000
	s_addc_u32 s45, s43, 0
	s_add_i32 s74, s64, s15
	s_add_i32 s73, s74, 0x2000
	s_add_i32 s71, 0, 0x18000
	s_add_i32 s70, 0, 0x1c000
	s_add_u32 s38, s40, 0x10000
	s_addc_u32 s39, s41, 0
	s_add_i32 s69, s71, s15
	s_add_i32 s67, s69, 0x2000
	s_add_u32 s36, s42, 0x10080
	s_addc_u32 s37, s43, 0
	s_add_i32 s68, s70, s15
	s_add_i32 s66, s68, 0x2000
	v_lshl_add_u64 v[208:209], s[76:77], 0, v[164:165]
	ds_read_b128 v[170:173], v183
	ds_read_b128 v[174:177], v183 offset:1024
	ds_read_b128 v[184:187], v183 offset:2048
	ds_read_b128 v[188:191], v183 offset:3072
	ds_read_b128 v[192:195], v183 offset:4096
	ds_read_b128 v[196:199], v183 offset:5120
	ds_read_b128 v[200:203], v183 offset:6144
	ds_read_b128 v[204:207], v183 offset:7168
	global_load_lds_dwordx4 v[208:209], off
	v_lshl_add_u64 v[208:209], s[76:77], 0, v[162:163]
	s_mov_b32 m0, s78
	s_nop 0
	global_load_lds_dwordx4 v[208:209], off
	s_waitcnt vmcnt(8)
	s_waitcnt lgkmcnt(0)
	s_barrier
	s_setprio 1
	s_waitcnt lgkmcnt(0)
	v_mfma_scale_f32_16x16x128_f8f6f4 v[158:161], v[26:33], v[170:177], v[158:161], v1, v1 op_sel_hi:[0,0,0]
	v_mfma_scale_f32_16x16x128_f8f6f4 v[154:157], v[18:25], v[170:177], v[154:157], v1, v1 op_sel_hi:[0,0,0]
	v_mfma_scale_f32_16x16x128_f8f6f4 v[138:141], v[18:25], v[184:191], v[138:141], v1, v1 op_sel_hi:[0,0,0]
	v_mfma_scale_f32_16x16x128_f8f6f4 v[142:145], v[26:33], v[184:191], v[142:145], v1, v1 op_sel_hi:[0,0,0]
	v_mfma_scale_f32_16x16x128_f8f6f4 v[126:129], v[26:33], v[192:199], v[126:129], v1, v1 op_sel_hi:[0,0,0]
	v_mfma_scale_f32_16x16x128_f8f6f4 v[122:125], v[18:25], v[192:199], v[122:125], v1, v1 op_sel_hi:[0,0,0]
	v_mfma_scale_f32_16x16x128_f8f6f4 v[106:109], v[18:25], v[200:207], v[106:109], v1, v1 op_sel_hi:[0,0,0]
	v_mfma_scale_f32_16x16x128_f8f6f4 v[110:113], v[26:33], v[200:207], v[110:113], v1, v1 op_sel_hi:[0,0,0]
	s_setprio 0
	s_setprio 1
	v_mfma_scale_f32_16x16x128_f8f6f4 v[102:105], v[10:17], v[200:207], v[102:105], v1, v1 op_sel_hi:[0,0,0]
	v_mfma_scale_f32_16x16x128_f8f6f4 v[98:101], v[2:9], v[200:207], v[98:101], v1, v1 op_sel_hi:[0,0,0]
	v_mfma_scale_f32_16x16x128_f8f6f4 v[146:149], v[2:9], v[170:177], v[146:149], v1, v1 op_sel_hi:[0,0,0]
	v_mfma_scale_f32_16x16x128_f8f6f4 v[150:153], v[10:17], v[170:177], v[150:153], v1, v1 op_sel_hi:[0,0,0]
	v_mfma_scale_f32_16x16x128_f8f6f4 v[134:137], v[10:17], v[184:191], v[134:137], v1, v1 op_sel_hi:[0,0,0]
	v_mfma_scale_f32_16x16x128_f8f6f4 v[130:133], v[2:9], v[184:191], v[130:133], v1, v1 op_sel_hi:[0,0,0]
	v_mfma_scale_f32_16x16x128_f8f6f4 v[114:117], v[2:9], v[192:199], v[114:117], v1, v1 op_sel_hi:[0,0,0]
	v_mfma_scale_f32_16x16x128_f8f6f4 v[118:121], v[10:17], v[192:199], v[118:121], v1, v1 op_sel_hi:[0,0,0]
	s_setprio 0
	s_barrier
	s_mov_b32 m0, s75
	v_lshl_add_u64 v[170:171], s[42:43], 0, v[164:165]
	ds_read_b128 v[184:187], v183 offset:16384
	ds_read_b128 v[188:191], v183 offset:17408
	ds_read_b128 v[192:195], v183 offset:18432
	ds_read_b128 v[196:199], v183 offset:19456
	ds_read_b128 v[200:203], v183 offset:20480
	ds_read_b128 v[204:207], v183 offset:21504
	ds_read_b128 v[208:211], v183 offset:22528
	ds_read_b128 v[212:215], v183 offset:23552
	global_load_lds_dwordx4 v[170:171], off
	v_lshl_add_u64 v[172:173], s[42:43], 0, v[162:163]
	s_mov_b32 m0, s72
	v_lshl_add_u64 v[174:175], s[44:45], 0, v[164:165]
	global_load_lds_dwordx4 v[172:173], off
	s_mov_b32 m0, s74
	v_lshl_add_u64 v[176:177], s[40:41], 0, v[162:163]
	global_load_lds_dwordx4 v[174:175], off
	v_lshl_add_u64 v[174:175], s[44:45], 0, v[162:163]
	s_mov_b32 m0, s73
	s_nop 0
	global_load_lds_dwordx4 v[174:175], off
	v_lshl_add_u64 v[174:175], s[40:41], 0, v[164:165]
	s_mov_b32 m0, s27
	s_nop 0
	global_load_lds_dwordx4 v[174:175], off
	s_mov_b32 m0, s49
	s_nop 0
	global_load_lds_dwordx4 v[176:177], off
	s_waitcnt vmcnt(8)
	s_waitcnt lgkmcnt(0)
	s_barrier
	s_setprio 1
	s_waitcnt lgkmcnt(0)
	v_mfma_scale_f32_16x16x128_f8f6f4 v[78:81], v[26:33], v[192:199], v[78:81], v1, v1 op_sel_hi:[0,0,0]
	v_mfma_scale_f32_16x16x128_f8f6f4 v[74:77], v[18:25], v[192:199], v[74:77], v1, v1 op_sel_hi:[0,0,0]
	v_mfma_scale_f32_16x16x128_f8f6f4 v[90:93], v[18:25], v[184:191], v[90:93], v1, v1 op_sel_hi:[0,0,0]
	v_mfma_scale_f32_16x16x128_f8f6f4 v[94:97], v[26:33], v[184:191], v[94:97], v1, v1 op_sel_hi:[0,0,0]
	v_mfma_scale_f32_16x16x128_f8f6f4 v[62:65], v[26:33], v[200:207], v[62:65], v1, v1 op_sel_hi:[0,0,0]
	v_mfma_scale_f32_16x16x128_f8f6f4 v[58:61], v[18:25], v[200:207], v[58:61], v1, v1 op_sel_hi:[0,0,0]
	v_mfma_scale_f32_16x16x128_f8f6f4 v[42:45], v[18:25], v[208:215], v[42:45], v1, v1 op_sel_hi:[0,0,0]
	v_mfma_scale_f32_16x16x128_f8f6f4 v[54:57], v[26:33], v[208:215], v[54:57], v1, v1 op_sel_hi:[0,0,0]
	s_setprio 0
	s_setprio 1
	v_mfma_scale_f32_16x16x128_f8f6f4 v[38:41], v[10:17], v[208:215], v[38:41], v1, v1 op_sel_hi:[0,0,0]
	v_mfma_scale_f32_16x16x128_f8f6f4 v[34:37], v[2:9], v[208:215], v[34:37], v1, v1 op_sel_hi:[0,0,0]
	v_mfma_scale_f32_16x16x128_f8f6f4 v[82:85], v[2:9], v[184:191], v[82:85], v1, v1 op_sel_hi:[0,0,0]
	v_mfma_scale_f32_16x16x128_f8f6f4 v[86:89], v[10:17], v[184:191], v[86:89], v1, v1 op_sel_hi:[0,0,0]
	v_mfma_scale_f32_16x16x128_f8f6f4 v[70:73], v[10:17], v[192:199], v[70:73], v1, v1 op_sel_hi:[0,0,0]
	v_mfma_scale_f32_16x16x128_f8f6f4 v[66:69], v[2:9], v[192:199], v[66:69], v1, v1 op_sel_hi:[0,0,0]
	v_mfma_scale_f32_16x16x128_f8f6f4 v[46:49], v[2:9], v[200:207], v[46:49], v1, v1 op_sel_hi:[0,0,0]
	v_mfma_scale_f32_16x16x128_f8f6f4 v[50:53], v[10:17], v[200:207], v[50:53], v1, v1 op_sel_hi:[0,0,0]
	s_setprio 0
	s_barrier
	v_add_u32_e32 v14, s71, v179
	v_add_u32_e32 v30, s70, v179
	ds_read_b128 v[2:5], v14
	ds_read_b128 v[6:9], v14 offset:1024
	ds_read_b128 v[10:13], v14 offset:2048
	ds_read_b128 v[14:17], v14 offset:3072
	ds_read_b128 v[18:21], v30
	ds_read_b128 v[22:25], v30 offset:1024
	ds_read_b128 v[26:29], v30 offset:2048
	ds_read_b128 v[30:33], v30 offset:3072
	s_mov_b32 m0, s50
	v_lshl_add_u64 v[216:217], s[38:39], 0, v[164:165]
	ds_read_b128 v[184:187], v183 offset:32768
	ds_read_b128 v[188:191], v183 offset:33792
	ds_read_b128 v[192:195], v183 offset:34816
	ds_read_b128 v[196:199], v183 offset:35840
	ds_read_b128 v[200:203], v183 offset:36864
	ds_read_b128 v[204:207], v183 offset:37888
	ds_read_b128 v[208:211], v183 offset:38912
	ds_read_b128 v[212:215], v183 offset:39936
	global_load_lds_dwordx4 v[216:217], off
	v_lshl_add_u64 v[216:217], s[38:39], 0, v[162:163]
	s_mov_b32 m0, s51
	s_nop 0
	global_load_lds_dwordx4 v[216:217], off
	s_waitcnt vmcnt(8)
	s_waitcnt lgkmcnt(0)
	s_barrier
	s_setprio 1
	s_waitcnt lgkmcnt(0)
	v_mfma_scale_f32_16x16x128_f8f6f4 v[122:125], v[10:17], v[200:207], v[122:125], v1, v1 op_sel_hi:[0,0,0]
	v_mfma_scale_f32_16x16x128_f8f6f4 v[126:129], v[2:9], v[200:207], v[126:129], v1, v1 op_sel_hi:[0,0,0]
	v_mfma_scale_f32_16x16x128_f8f6f4 v[158:161], v[2:9], v[184:191], v[158:161], v1, v1 op_sel_hi:[0,0,0]
	v_mfma_scale_f32_16x16x128_f8f6f4 v[154:157], v[10:17], v[184:191], v[154:157], v1, v1 op_sel_hi:[0,0,0]
	v_mfma_scale_f32_16x16x128_f8f6f4 v[138:141], v[10:17], v[192:199], v[138:141], v1, v1 op_sel_hi:[0,0,0]
	v_mfma_scale_f32_16x16x128_f8f6f4 v[142:145], v[2:9], v[192:199], v[142:145], v1, v1 op_sel_hi:[0,0,0]
	v_mfma_scale_f32_16x16x128_f8f6f4 v[110:113], v[2:9], v[208:215], v[110:113], v1, v1 op_sel_hi:[0,0,0]
	v_mfma_scale_f32_16x16x128_f8f6f4 v[106:109], v[10:17], v[208:215], v[106:109], v1, v1 op_sel_hi:[0,0,0]
	s_setprio 0
	s_setprio 1
	v_mfma_scale_f32_16x16x128_f8f6f4 v[102:105], v[18:25], v[208:215], v[102:105], v1, v1 op_sel_hi:[0,0,0]
	v_mfma_scale_f32_16x16x128_f8f6f4 v[98:101], v[26:33], v[208:215], v[98:101], v1, v1 op_sel_hi:[0,0,0]
	v_mfma_scale_f32_16x16x128_f8f6f4 v[146:149], v[26:33], v[184:191], v[146:149], v1, v1 op_sel_hi:[0,0,0]
	v_mfma_scale_f32_16x16x128_f8f6f4 v[150:153], v[18:25], v[184:191], v[150:153], v1, v1 op_sel_hi:[0,0,0]
	v_mfma_scale_f32_16x16x128_f8f6f4 v[134:137], v[18:25], v[192:199], v[134:137], v1, v1 op_sel_hi:[0,0,0]
	v_mfma_scale_f32_16x16x128_f8f6f4 v[130:133], v[26:33], v[192:199], v[130:133], v1, v1 op_sel_hi:[0,0,0]
	v_mfma_scale_f32_16x16x128_f8f6f4 v[114:117], v[26:33], v[200:207], v[114:117], v1, v1 op_sel_hi:[0,0,0]
	v_mfma_scale_f32_16x16x128_f8f6f4 v[118:121], v[18:25], v[200:207], v[118:121], v1, v1 op_sel_hi:[0,0,0]
	s_setprio 0
	s_barrier
	s_mov_b32 m0, s69
	v_lshl_add_u64 v[170:171], v[170:171], 0, s[8:9]
	ds_read_b128 v[184:187], v183 offset:49152
	ds_read_b128 v[188:191], v183 offset:50176
	ds_read_b128 v[192:195], v183 offset:51200
	ds_read_b128 v[196:199], v183 offset:52224
	ds_read_b128 v[200:203], v183 offset:53248
	ds_read_b128 v[204:207], v183 offset:54272
	ds_read_b128 v[208:211], v183 offset:55296
	ds_read_b128 v[212:215], v183 offset:56320
	global_load_lds_dwordx4 v[170:171], off
	v_lshl_add_u64 v[170:171], v[172:173], 0, s[8:9]
	s_mov_b32 m0, s67
	s_nop 0
	global_load_lds_dwordx4 v[170:171], off
	v_lshl_add_u64 v[170:171], s[36:37], 0, v[164:165]
	s_mov_b32 m0, s68
	s_nop 0
	global_load_lds_dwordx4 v[170:171], off
	v_lshl_add_u64 v[170:171], s[36:37], 0, v[162:163]
	s_mov_b32 m0, s66
	s_nop 0
	global_load_lds_dwordx4 v[170:171], off
	v_lshl_add_u64 v[170:171], v[174:175], 0, s[8:9]
	s_mov_b32 m0, s61
	s_nop 0
	global_load_lds_dwordx4 v[170:171], off
	v_lshl_add_u64 v[170:171], v[176:177], 0, s[8:9]
	s_mov_b32 m0, s62
	s_nop 0
	global_load_lds_dwordx4 v[170:171], off
	s_waitcnt vmcnt(8)
	s_waitcnt lgkmcnt(0)
	s_barrier
	s_setprio 1
	s_waitcnt lgkmcnt(0)
	v_mfma_scale_f32_16x16x128_f8f6f4 v[62:65], v[2:9], v[200:207], v[62:65], v1, v1 op_sel_hi:[0,0,0]
	v_mfma_scale_f32_16x16x128_f8f6f4 v[58:61], v[10:17], v[200:207], v[58:61], v1, v1 op_sel_hi:[0,0,0]
	v_mfma_scale_f32_16x16x128_f8f6f4 v[90:93], v[10:17], v[184:191], v[90:93], v1, v1 op_sel_hi:[0,0,0]
	v_mfma_scale_f32_16x16x128_f8f6f4 v[94:97], v[2:9], v[184:191], v[94:97], v1, v1 op_sel_hi:[0,0,0]
	v_mfma_scale_f32_16x16x128_f8f6f4 v[78:81], v[2:9], v[192:199], v[78:81], v1, v1 op_sel_hi:[0,0,0]
	v_mfma_scale_f32_16x16x128_f8f6f4 v[74:77], v[10:17], v[192:199], v[74:77], v1, v1 op_sel_hi:[0,0,0]
	v_mfma_scale_f32_16x16x128_f8f6f4 v[42:45], v[10:17], v[208:215], v[42:45], v1, v1 op_sel_hi:[0,0,0]
	v_mfma_scale_f32_16x16x128_f8f6f4 v[54:57], v[2:9], v[208:215], v[54:57], v1, v1 op_sel_hi:[0,0,0]
	s_setprio 0
	s_setprio 1
	v_mfma_scale_f32_16x16x128_f8f6f4 v[38:41], v[18:25], v[208:215], v[38:41], v1, v1 op_sel_hi:[0,0,0]
	v_mfma_scale_f32_16x16x128_f8f6f4 v[34:37], v[26:33], v[208:215], v[34:37], v1, v1 op_sel_hi:[0,0,0]
	v_mfma_scale_f32_16x16x128_f8f6f4 v[82:85], v[26:33], v[184:191], v[82:85], v1, v1 op_sel_hi:[0,0,0]
	v_mfma_scale_f32_16x16x128_f8f6f4 v[86:89], v[18:25], v[184:191], v[86:89], v1, v1 op_sel_hi:[0,0,0]
	v_mfma_scale_f32_16x16x128_f8f6f4 v[70:73], v[18:25], v[192:199], v[70:73], v1, v1 op_sel_hi:[0,0,0]
	v_mfma_scale_f32_16x16x128_f8f6f4 v[66:69], v[26:33], v[192:199], v[66:69], v1, v1 op_sel_hi:[0,0,0]
	v_mfma_scale_f32_16x16x128_f8f6f4 v[46:49], v[26:33], v[200:207], v[46:49], v1, v1 op_sel_hi:[0,0,0]
	v_mfma_scale_f32_16x16x128_f8f6f4 v[50:53], v[18:25], v[200:207], v[50:53], v1, v1 op_sel_hi:[0,0,0]
	s_setprio 0
	s_barrier
	s_movk_i32 s38, 0x100
	s_andn2_b64 vcc, exec, s[34:35]
	s_mov_b64 s[36:37], -1
	s_mov_b64 s[34:35], 0
	s_cbranch_vccz .LBB0_1558
	s_and_b64 vcc, exec, s[12:13]
	s_cbranch_vccz .LBB0_1561
	s_barrier

.LBB0_1681:
	ds_read_b128 v[26:29], v189
	ds_read_b128 v[30:33], v189 offset:1024
	ds_read_b128 v[18:21], v189 offset:2048
	ds_read_b128 v[22:25], v189 offset:3072
	ds_read_b128 v[10:13], v190
	ds_read_b128 v[14:17], v190 offset:1024
	ds_read_b128 v[2:5], v190 offset:2048
	ds_read_b128 v[6:9], v190 offset:3072
	s_add_u32 s34, s30, 0xfff80080
	s_addc_u32 s35, s31, -1
	s_cmp_eq_u32 s60, 28
	s_cselect_b32 s37, s18, s35
	s_cselect_b32 s36, s19, s34
	s_cselect_b32 s35, s21, s59
	s_cselect_b32 s34, s23, s58
	s_mov_b32 m0, s43
	s_nop 0
	global_load_lds_dwordx4 v168, s[100:101]
	s_mov_b32 m0, s44
	s_nop 0
	global_load_lds_dwordx4 v164, s[100:101]
	s_add_i32 m0, s29, 0xc000
	ds_read_b128 v[178:181], v191
	ds_read_b128 v[182:185], v191 offset:1024
	ds_read_b128 v[194:197], v191 offset:2048
	ds_read_b128 v[198:201], v191 offset:3072
	ds_read_b128 v[202:205], v191 offset:4096
	ds_read_b128 v[206:209], v191 offset:5120
	ds_read_b128 v[210:213], v191 offset:6144
	ds_read_b128 v[214:217], v191 offset:7168
	global_load_lds_dwordx4 v170, s[30:31]
	s_add_i32 m0, s29, 0xe000
	s_nop 0
	global_load_lds_dwordx4 v172, s[30:31]
	s_waitcnt vmcnt(8)
	s_waitcnt lgkmcnt(0)
	s_barrier
	s_setprio 1
	s_waitcnt lgkmcnt(0)
	v_mfma_scale_f32_16x16x128_f8f6f4 v[158:161], v[26:33], v[178:185], v[158:161], v1, v1 op_sel_hi:[0,0,0]
	v_mfma_scale_f32_16x16x128_f8f6f4 v[154:157], v[18:25], v[178:185], v[154:157], v1, v1 op_sel_hi:[0,0,0]
	v_mfma_scale_f32_16x16x128_f8f6f4 v[138:141], v[18:25], v[194:201], v[138:141], v1, v1 op_sel_hi:[0,0,0]
	v_mfma_scale_f32_16x16x128_f8f6f4 v[142:145], v[26:33], v[194:201], v[142:145], v1, v1 op_sel_hi:[0,0,0]
	v_mfma_scale_f32_16x16x128_f8f6f4 v[126:129], v[26:33], v[202:209], v[126:129], v1, v1 op_sel_hi:[0,0,0]
	v_mfma_scale_f32_16x16x128_f8f6f4 v[122:125], v[18:25], v[202:209], v[122:125], v1, v1 op_sel_hi:[0,0,0]
	v_mfma_scale_f32_16x16x128_f8f6f4 v[106:109], v[18:25], v[210:217], v[106:109], v1, v1 op_sel_hi:[0,0,0]
	v_mfma_scale_f32_16x16x128_f8f6f4 v[110:113], v[26:33], v[210:217], v[110:113], v1, v1 op_sel_hi:[0,0,0]
	s_setprio 0
	s_setprio 1
	v_mfma_scale_f32_16x16x128_f8f6f4 v[102:105], v[10:17], v[210:217], v[102:105], v1, v1 op_sel_hi:[0,0,0]
	v_mfma_scale_f32_16x16x128_f8f6f4 v[98:101], v[2:9], v[210:217], v[98:101], v1, v1 op_sel_hi:[0,0,0]
	v_mfma_scale_f32_16x16x128_f8f6f4 v[146:149], v[2:9], v[178:185], v[146:149], v1, v1 op_sel_hi:[0,0,0]
	v_mfma_scale_f32_16x16x128_f8f6f4 v[150:153], v[10:17], v[178:185], v[150:153], v1, v1 op_sel_hi:[0,0,0]
	v_mfma_scale_f32_16x16x128_f8f6f4 v[134:137], v[10:17], v[194:201], v[134:137], v1, v1 op_sel_hi:[0,0,0]
	v_mfma_scale_f32_16x16x128_f8f6f4 v[130:133], v[2:9], v[194:201], v[130:133], v1, v1 op_sel_hi:[0,0,0]
	v_mfma_scale_f32_16x16x128_f8f6f4 v[114:117], v[2:9], v[202:209], v[114:117], v1, v1 op_sel_hi:[0,0,0]
	v_mfma_scale_f32_16x16x128_f8f6f4 v[118:121], v[10:17], v[202:209], v[118:121], v1, v1 op_sel_hi:[0,0,0]
	s_setprio 0
	s_barrier
	s_add_i32 s61, s45, s3
	s_mov_b32 m0, s61
	ds_read_b128 v[194:197], v191 offset:16384
	ds_read_b128 v[198:201], v191 offset:17408
	ds_read_b128 v[202:205], v191 offset:18432
	ds_read_b128 v[206:209], v191 offset:19456
	ds_read_b128 v[210:213], v191 offset:20480
	ds_read_b128 v[214:217], v191 offset:21504
	ds_read_b128 v[218:221], v191 offset:22528
	ds_read_b128 v[222:225], v191 offset:23552
	global_load_lds_dwordx4 v166, s[34:35]
	s_add_i32 m0, s61, 0x2000
	s_add_u32 s62, s34, 0x80000
	s_addc_u32 s63, s35, 0
	s_add_i32 s61, s48, s3
	global_load_lds_dwordx4 v162, s[34:35]
	s_mov_b32 m0, s61
	s_nop 0
	global_load_lds_dwordx4 v166, s[62:63]
	s_add_i32 m0, s61, 0x2000
	s_nop 0
	global_load_lds_dwordx4 v162, s[62:63]
	s_waitcnt vmcnt(6)
	s_waitcnt lgkmcnt(0)
	s_barrier
	s_setprio 1
	s_waitcnt lgkmcnt(0)
	v_mfma_scale_f32_16x16x128_f8f6f4 v[78:81], v[26:33], v[202:209], v[78:81], v1, v1 op_sel_hi:[0,0,0]
	v_mfma_scale_f32_16x16x128_f8f6f4 v[74:77], v[18:25], v[202:209], v[74:77], v1, v1 op_sel_hi:[0,0,0]
	v_mfma_scale_f32_16x16x128_f8f6f4 v[90:93], v[18:25], v[194:201], v[90:93], v1, v1 op_sel_hi:[0,0,0]
	v_mfma_scale_f32_16x16x128_f8f6f4 v[94:97], v[26:33], v[194:201], v[94:97], v1, v1 op_sel_hi:[0,0,0]
	v_mfma_scale_f32_16x16x128_f8f6f4 v[62:65], v[26:33], v[210:217], v[62:65], v1, v1 op_sel_hi:[0,0,0]
	v_mfma_scale_f32_16x16x128_f8f6f4 v[58:61], v[18:25], v[210:217], v[58:61], v1, v1 op_sel_hi:[0,0,0]
	v_mfma_scale_f32_16x16x128_f8f6f4 v[42:45], v[18:25], v[218:225], v[42:45], v1, v1 op_sel_hi:[0,0,0]
	v_mfma_scale_f32_16x16x128_f8f6f4 v[46:49], v[26:33], v[218:225], v[46:49], v1, v1 op_sel_hi:[0,0,0]
	s_setprio 0
	s_setprio 1
	v_mfma_scale_f32_16x16x128_f8f6f4 v[38:41], v[10:17], v[218:225], v[38:41], v1, v1 op_sel_hi:[0,0,0]
	v_mfma_scale_f32_16x16x128_f8f6f4 v[34:37], v[2:9], v[218:225], v[34:37], v1, v1 op_sel_hi:[0,0,0]
	v_mfma_scale_f32_16x16x128_f8f6f4 v[82:85], v[2:9], v[194:201], v[82:85], v1, v1 op_sel_hi:[0,0,0]
	v_mfma_scale_f32_16x16x128_f8f6f4 v[86:89], v[10:17], v[194:201], v[86:89], v1, v1 op_sel_hi:[0,0,0]
	v_mfma_scale_f32_16x16x128_f8f6f4 v[70:73], v[10:17], v[202:209], v[70:73], v1, v1 op_sel_hi:[0,0,0]
	v_mfma_scale_f32_16x16x128_f8f6f4 v[66:69], v[2:9], v[202:209], v[66:69], v1, v1 op_sel_hi:[0,0,0]
	v_mfma_scale_f32_16x16x128_f8f6f4 v[50:53], v[2:9], v[210:217], v[50:53], v1, v1 op_sel_hi:[0,0,0]
	v_mfma_scale_f32_16x16x128_f8f6f4 v[54:57], v[10:17], v[210:217], v[54:57], v1, v1 op_sel_hi:[0,0,0]
	s_setprio 0
	s_barrier
	s_add_i32 s61, 0, 0x18000
	s_add_i32 s62, 0, 0x1c000
	v_add_u32_e32 v14, s61, v187
	v_add_u32_e32 v30, s62, v187
	ds_read_b128 v[2:5], v14
	ds_read_b128 v[6:9], v14 offset:1024
	ds_read_b128 v[10:13], v14 offset:2048
	ds_read_b128 v[14:17], v14 offset:3072
	ds_read_b128 v[18:21], v30
	ds_read_b128 v[22:25], v30 offset:1024
	ds_read_b128 v[26:29], v30 offset:2048
	ds_read_b128 v[30:33], v30 offset:3072
	s_mov_b32 m0, s29
	s_nop 0
	global_load_lds_dwordx4 v168, s[36:37]
	s_mov_b32 m0, s38
	s_nop 0
	global_load_lds_dwordx4 v164, s[36:37]
	s_add_u32 s36, s36, 0x80000
	s_addc_u32 s37, s37, 0
	s_add_u32 s100, s36, 0xfff80080
	s_addc_u32 s101, s37, -1
	s_mov_b32 m0, s39
	ds_read_b128 v[194:197], v191 offset:32768
	ds_read_b128 v[198:201], v191 offset:33792
	ds_read_b128 v[202:205], v191 offset:34816
	ds_read_b128 v[206:209], v191 offset:35840
	ds_read_b128 v[210:213], v191 offset:36864
	ds_read_b128 v[214:217], v191 offset:37888
	ds_read_b128 v[218:221], v191 offset:38912
	ds_read_b128 v[222:225], v191 offset:39936
	global_load_lds_dwordx4 v168, s[36:37]
	s_mov_b32 m0, s40
	s_nop 0
	global_load_lds_dwordx4 v164, s[36:37]
	s_waitcnt vmcnt(8)
	s_waitcnt lgkmcnt(0)
	s_barrier
	s_setprio 1
	s_waitcnt lgkmcnt(0)
	v_mfma_scale_f32_16x16x128_f8f6f4 v[122:125], v[10:17], v[210:217], v[122:125], v1, v1 op_sel_hi:[0,0,0]
	v_mfma_scale_f32_16x16x128_f8f6f4 v[126:129], v[2:9], v[210:217], v[126:129], v1, v1 op_sel_hi:[0,0,0]
	v_mfma_scale_f32_16x16x128_f8f6f4 v[158:161], v[2:9], v[194:201], v[158:161], v1, v1 op_sel_hi:[0,0,0]
	v_mfma_scale_f32_16x16x128_f8f6f4 v[154:157], v[10:17], v[194:201], v[154:157], v1, v1 op_sel_hi:[0,0,0]
	v_mfma_scale_f32_16x16x128_f8f6f4 v[138:141], v[10:17], v[202:209], v[138:141], v1, v1 op_sel_hi:[0,0,0]
	v_mfma_scale_f32_16x16x128_f8f6f4 v[142:145], v[2:9], v[202:209], v[142:145], v1, v1 op_sel_hi:[0,0,0]
	v_mfma_scale_f32_16x16x128_f8f6f4 v[110:113], v[2:9], v[218:225], v[110:113], v1, v1 op_sel_hi:[0,0,0]
	v_mfma_scale_f32_16x16x128_f8f6f4 v[106:109], v[10:17], v[218:225], v[106:109], v1, v1 op_sel_hi:[0,0,0]
	s_setprio 0
	s_setprio 1
	v_mfma_scale_f32_16x16x128_f8f6f4 v[102:105], v[18:25], v[218:225], v[102:105], v1, v1 op_sel_hi:[0,0,0]
	v_mfma_scale_f32_16x16x128_f8f6f4 v[98:101], v[26:33], v[218:225], v[98:101], v1, v1 op_sel_hi:[0,0,0]
	v_mfma_scale_f32_16x16x128_f8f6f4 v[146:149], v[26:33], v[194:201], v[146:149], v1, v1 op_sel_hi:[0,0,0]
	v_mfma_scale_f32_16x16x128_f8f6f4 v[150:153], v[18:25], v[194:201], v[150:153], v1, v1 op_sel_hi:[0,0,0]
	v_mfma_scale_f32_16x16x128_f8f6f4 v[134:137], v[18:25], v[202:209], v[134:137], v1, v1 op_sel_hi:[0,0,0]
	v_mfma_scale_f32_16x16x128_f8f6f4 v[130:133], v[26:33], v[202:209], v[130:133], v1, v1 op_sel_hi:[0,0,0]
	v_mfma_scale_f32_16x16x128_f8f6f4 v[114:117], v[26:33], v[210:217], v[114:117], v1, v1 op_sel_hi:[0,0,0]
	v_mfma_scale_f32_16x16x128_f8f6f4 v[118:121], v[18:25], v[210:217], v[118:121], v1, v1 op_sel_hi:[0,0,0]
	s_setprio 0
	s_barrier
	s_add_i32 s36, s61, s3
	s_mov_b32 m0, s36
	s_add_u32 s98, s34, 0x80
	s_addc_u32 s99, s35, 0
	ds_read_b128 v[194:197], v191 offset:49152
	ds_read_b128 v[198:201], v191 offset:50176
	ds_read_b128 v[202:205], v191 offset:51200
	ds_read_b128 v[206:209], v191 offset:52224
	ds_read_b128 v[210:213], v191 offset:53248
	ds_read_b128 v[214:217], v191 offset:54272
	ds_read_b128 v[218:221], v191 offset:55296
	ds_read_b128 v[222:225], v191 offset:56320
	global_load_lds_dwordx4 v166, s[98:99]
	s_add_i32 m0, s36, 0x2000
	s_add_u32 s34, s34, 0x80080
	s_addc_u32 s35, s35, 0
	s_add_i32 s36, s62, s3
	global_load_lds_dwordx4 v162, s[98:99]
	s_mov_b32 m0, s36
	s_nop 0
	global_load_lds_dwordx4 v166, s[34:35]
	s_add_i32 m0, s36, 0x2000
	s_nop 0
	global_load_lds_dwordx4 v162, s[34:35]
	s_waitcnt vmcnt(6)
	s_waitcnt lgkmcnt(0)
	s_barrier
	s_setprio 1
	s_waitcnt lgkmcnt(0)
	v_mfma_scale_f32_16x16x128_f8f6f4 v[62:65], v[2:9], v[210:217], v[62:65], v1, v1 op_sel_hi:[0,0,0]
	v_mfma_scale_f32_16x16x128_f8f6f4 v[58:61], v[10:17], v[210:217], v[58:61], v1, v1 op_sel_hi:[0,0,0]
	v_mfma_scale_f32_16x16x128_f8f6f4 v[90:93], v[10:17], v[194:201], v[90:93], v1, v1 op_sel_hi:[0,0,0]
	v_mfma_scale_f32_16x16x128_f8f6f4 v[94:97], v[2:9], v[194:201], v[94:97], v1, v1 op_sel_hi:[0,0,0]
	v_mfma_scale_f32_16x16x128_f8f6f4 v[78:81], v[2:9], v[202:209], v[78:81], v1, v1 op_sel_hi:[0,0,0]
	v_mfma_scale_f32_16x16x128_f8f6f4 v[74:77], v[10:17], v[202:209], v[74:77], v1, v1 op_sel_hi:[0,0,0]
	v_mfma_scale_f32_16x16x128_f8f6f4 v[42:45], v[10:17], v[218:225], v[42:45], v1, v1 op_sel_hi:[0,0,0]
	v_mfma_scale_f32_16x16x128_f8f6f4 v[46:49], v[2:9], v[218:225], v[46:49], v1, v1 op_sel_hi:[0,0,0]
	s_setprio 0
	s_setprio 1
	v_mfma_scale_f32_16x16x128_f8f6f4 v[38:41], v[18:25], v[218:225], v[38:41], v1, v1 op_sel_hi:[0,0,0]
	v_mfma_scale_f32_16x16x128_f8f6f4 v[34:37], v[26:33], v[218:225], v[34:37], v1, v1 op_sel_hi:[0,0,0]
	v_mfma_scale_f32_16x16x128_f8f6f4 v[82:85], v[26:33], v[194:201], v[82:85], v1, v1 op_sel_hi:[0,0,0]
	v_mfma_scale_f32_16x16x128_f8f6f4 v[86:89], v[18:25], v[194:201], v[86:89], v1, v1 op_sel_hi:[0,0,0]
	v_mfma_scale_f32_16x16x128_f8f6f4 v[70:73], v[18:25], v[202:209], v[70:73], v1, v1 op_sel_hi:[0,0,0]
	v_mfma_scale_f32_16x16x128_f8f6f4 v[66:69], v[26:33], v[202:209], v[66:69], v1, v1 op_sel_hi:[0,0,0]
	v_mfma_scale_f32_16x16x128_f8f6f4 v[50:53], v[26:33], v[210:217], v[50:53], v1, v1 op_sel_hi:[0,0,0]
	v_mfma_scale_f32_16x16x128_f8f6f4 v[54:57], v[18:25], v[210:217], v[54:57], v1, v1 op_sel_hi:[0,0,0]
	s_setprio 0
	s_barrier
	s_add_i32 s60, s60, 2
	s_add_u32 s30, s30, 0x100
	s_addc_u32 s31, s31, 0
	s_add_u32 s58, s58, 0x100
	s_addc_u32 s59, s59, 0
	s_cmp_gt_u32 s60, 29
	s_cbranch_scc0 .LBB0_1681
	s_and_b64 vcc, exec, s[12:13]
	s_cbranch_vccz .LBB0_1684
	s_barrier

.LBB0_1745:
	s_add_u32 s8, s49, s6
	s_addc_u32 s9, s50, s7
	s_add_u32 s8, s8, 0x32800100
	s_addc_u32 s9, s9, 0
	s_add_u32 s73, s51, s6
	s_addc_u32 s74, s54, s7
	s_add_i32 s72, 0, 0x10000
	s_cmpk_eq_i32 s6, 0x2a00
	s_cselect_b32 s37, s5, s9
	s_cselect_b32 s36, s4, s8
	s_cselect_b32 s9, s13, s74
	s_cselect_b32 s8, s12, s73
	s_add_i32 s73, 0, 0x14000
	v_add_u32_e32 v2, s72, v188
	v_add_u32_e32 v6, s73, v188
	ds_read_b128 v[26:29], v2
	ds_read_b128 v[30:33], v2 offset:1024
	ds_read_b128 v[18:21], v2 offset:2048
	ds_read_b128 v[22:25], v2 offset:3072
	ds_read_b128 v[10:13], v6
	ds_read_b128 v[14:17], v6 offset:1024
	ds_read_b128 v[2:5], v6 offset:2048
	ds_read_b128 v[6:9], v6 offset:3072
	v_lshl_add_u64 v[214:215], v[168:169], 0, s[6:7]
	s_add_i32 m0, s64, 0xc000
	ds_read_b128 v[172:175], v189
	ds_read_b128 v[176:179], v189 offset:1024
	ds_read_b128 v[190:193], v189 offset:2048
	ds_read_b128 v[194:197], v189 offset:3072
	ds_read_b128 v[198:201], v189 offset:4096
	ds_read_b128 v[202:205], v189 offset:5120
	ds_read_b128 v[206:209], v189 offset:6144
	ds_read_b128 v[210:213], v189 offset:7168
	global_load_lds_dwordx4 v[214:215], off
	v_lshl_add_u64 v[214:215], v[170:171], 0, s[6:7]
	s_add_i32 m0, s64, 0xe000
	s_nop 0
	global_load_lds_dwordx4 v[214:215], off
	s_waitcnt vmcnt(8)
	s_waitcnt lgkmcnt(0)
	s_barrier
	s_setprio 1
	s_waitcnt lgkmcnt(0)
	v_mfma_scale_f32_16x16x128_f8f6f4 v[158:161], v[26:33], v[172:179], v[158:161], v187, v187 op_sel_hi:[0,0,0]
	v_mfma_scale_f32_16x16x128_f8f6f4 v[154:157], v[18:25], v[172:179], v[154:157], v187, v187 op_sel_hi:[0,0,0]
	v_mfma_scale_f32_16x16x128_f8f6f4 v[118:121], v[18:25], v[190:197], v[118:121], v187, v187 op_sel_hi:[0,0,0]
	v_mfma_scale_f32_16x16x128_f8f6f4 v[122:125], v[26:33], v[190:197], v[122:125], v187, v187 op_sel_hi:[0,0,0]
	v_mfma_scale_f32_16x16x128_f8f6f4 v[126:129], v[26:33], v[198:205], v[126:129], v187, v187 op_sel_hi:[0,0,0]
	v_mfma_scale_f32_16x16x128_f8f6f4 v[114:117], v[18:25], v[198:205], v[114:117], v187, v187 op_sel_hi:[0,0,0]
	v_mfma_scale_f32_16x16x128_f8f6f4 v[106:109], v[18:25], v[206:213], v[106:109], v187, v187 op_sel_hi:[0,0,0]
	v_mfma_scale_f32_16x16x128_f8f6f4 v[110:113], v[26:33], v[206:213], v[110:113], v187, v187 op_sel_hi:[0,0,0]
	s_setprio 0
	s_setprio 1
	v_mfma_scale_f32_16x16x128_f8f6f4 v[102:105], v[10:17], v[206:213], v[102:105], v187, v187 op_sel_hi:[0,0,0]
	v_mfma_scale_f32_16x16x128_f8f6f4 v[98:101], v[2:9], v[206:213], v[98:101], v187, v187 op_sel_hi:[0,0,0]
	v_mfma_scale_f32_16x16x128_f8f6f4 v[146:149], v[2:9], v[172:179], v[146:149], v187, v187 op_sel_hi:[0,0,0]
	v_mfma_scale_f32_16x16x128_f8f6f4 v[150:153], v[10:17], v[172:179], v[150:153], v187, v187 op_sel_hi:[0,0,0]
	v_mfma_scale_f32_16x16x128_f8f6f4 v[142:145], v[10:17], v[190:197], v[142:145], v187, v187 op_sel_hi:[0,0,0]
	v_mfma_scale_f32_16x16x128_f8f6f4 v[138:141], v[2:9], v[190:197], v[138:141], v187, v187 op_sel_hi:[0,0,0]
	v_mfma_scale_f32_16x16x128_f8f6f4 v[130:133], v[2:9], v[198:205], v[130:133], v187, v187 op_sel_hi:[0,0,0]
	v_mfma_scale_f32_16x16x128_f8f6f4 v[134:137], v[10:17], v[198:205], v[134:137], v187, v187 op_sel_hi:[0,0,0]
	s_setprio 0
	s_barrier
	s_add_i32 s72, s72, s43
	v_lshl_add_u64 v[172:173], s[8:9], 0, v[162:163]
	s_mov_b32 m0, s72
	ds_read_b128 v[190:193], v189 offset:16384
	ds_read_b128 v[194:197], v189 offset:17408
	ds_read_b128 v[198:201], v189 offset:18432
	ds_read_b128 v[202:205], v189 offset:19456
	ds_read_b128 v[206:209], v189 offset:20480
	ds_read_b128 v[210:213], v189 offset:21504
	ds_read_b128 v[214:217], v189 offset:22528
	ds_read_b128 v[218:221], v189 offset:23552
	global_load_lds_dwordx4 v[172:173], off
	s_add_i32 m0, s72, 0x2000
	s_add_u32 s74, s8, 0x158000
	v_lshl_add_u64 v[174:175], s[8:9], 0, v[166:167]
	s_addc_u32 s75, s9, 0
	s_add_i32 s72, s73, s43
	global_load_lds_dwordx4 v[174:175], off
	v_lshl_add_u64 v[176:177], s[74:75], 0, v[162:163]
	s_mov_b32 m0, s72
	v_lshl_add_u64 v[178:179], s[36:37], 0, v[166:167]
	global_load_lds_dwordx4 v[176:177], off
	v_lshl_add_u64 v[176:177], s[74:75], 0, v[166:167]
	s_add_i32 m0, s72, 0x2000
	s_nop 0
	global_load_lds_dwordx4 v[176:177], off
	v_lshl_add_u64 v[176:177], s[36:37], 0, v[162:163]
	s_mov_b32 m0, s64
	s_nop 0
	global_load_lds_dwordx4 v[176:177], off
	s_mov_b32 m0, s65
	s_nop 0
	global_load_lds_dwordx4 v[178:179], off
	s_waitcnt vmcnt(8)
	s_waitcnt lgkmcnt(0)
	s_barrier
	s_setprio 1
	s_waitcnt lgkmcnt(0)
	v_mfma_scale_f32_16x16x128_f8f6f4 v[78:81], v[26:33], v[198:205], v[78:81], v187, v187 op_sel_hi:[0,0,0]
	v_mfma_scale_f32_16x16x128_f8f6f4 v[74:77], v[18:25], v[198:205], v[74:77], v187, v187 op_sel_hi:[0,0,0]
	v_mfma_scale_f32_16x16x128_f8f6f4 v[90:93], v[18:25], v[190:197], v[90:93], v187, v187 op_sel_hi:[0,0,0]
	v_mfma_scale_f32_16x16x128_f8f6f4 v[94:97], v[26:33], v[190:197], v[94:97], v187, v187 op_sel_hi:[0,0,0]
	v_mfma_scale_f32_16x16x128_f8f6f4 v[62:65], v[26:33], v[206:213], v[62:65], v187, v187 op_sel_hi:[0,0,0]
	v_mfma_scale_f32_16x16x128_f8f6f4 v[58:61], v[18:25], v[206:213], v[58:61], v187, v187 op_sel_hi:[0,0,0]
	v_mfma_scale_f32_16x16x128_f8f6f4 v[42:45], v[18:25], v[214:221], v[42:45], v187, v187 op_sel_hi:[0,0,0]
	v_mfma_scale_f32_16x16x128_f8f6f4 v[46:49], v[26:33], v[214:221], v[46:49], v187, v187 op_sel_hi:[0,0,0]
	s_setprio 0
	s_setprio 1
	v_mfma_scale_f32_16x16x128_f8f6f4 v[38:41], v[10:17], v[214:221], v[38:41], v187, v187 op_sel_hi:[0,0,0]
	v_mfma_scale_f32_16x16x128_f8f6f4 v[34:37], v[2:9], v[214:221], v[34:37], v187, v187 op_sel_hi:[0,0,0]
	v_mfma_scale_f32_16x16x128_f8f6f4 v[82:85], v[2:9], v[190:197], v[82:85], v187, v187 op_sel_hi:[0,0,0]
	v_mfma_scale_f32_16x16x128_f8f6f4 v[86:89], v[10:17], v[190:197], v[86:89], v187, v187 op_sel_hi:[0,0,0]
	v_mfma_scale_f32_16x16x128_f8f6f4 v[70:73], v[10:17], v[198:205], v[70:73], v187, v187 op_sel_hi:[0,0,0]
	v_mfma_scale_f32_16x16x128_f8f6f4 v[66:69], v[2:9], v[198:205], v[66:69], v187, v187 op_sel_hi:[0,0,0]
	v_mfma_scale_f32_16x16x128_f8f6f4 v[50:53], v[2:9], v[206:213], v[50:53], v187, v187 op_sel_hi:[0,0,0]
	v_mfma_scale_f32_16x16x128_f8f6f4 v[54:57], v[10:17], v[206:213], v[54:57], v187, v187 op_sel_hi:[0,0,0]
	s_setprio 0
	s_barrier
	s_add_i32 s72, 0, 0x18000
	s_add_i32 s73, 0, 0x1c000
	v_add_u32_e32 v14, s72, v188
	v_add_u32_e32 v30, s73, v188
	ds_read_b128 v[2:5], v14
	ds_read_b128 v[6:9], v14 offset:1024
	ds_read_b128 v[10:13], v14 offset:2048
	ds_read_b128 v[14:17], v14 offset:3072
	ds_read_b128 v[18:21], v30
	ds_read_b128 v[22:25], v30 offset:1024
	ds_read_b128 v[26:29], v30 offset:2048
	ds_read_b128 v[30:33], v30 offset:3072
	s_add_u32 s36, s36, 0x158000
	s_addc_u32 s37, s37, 0
	s_mov_b32 m0, s66
	v_lshl_add_u64 v[222:223], s[36:37], 0, v[162:163]
	ds_read_b128 v[190:193], v189 offset:32768
	ds_read_b128 v[194:197], v189 offset:33792
	ds_read_b128 v[198:201], v189 offset:34816
	ds_read_b128 v[202:205], v189 offset:35840
	ds_read_b128 v[206:209], v189 offset:36864
	ds_read_b128 v[210:213], v189 offset:37888
	ds_read_b128 v[214:217], v189 offset:38912
	ds_read_b128 v[218:221], v189 offset:39936
	global_load_lds_dwordx4 v[222:223], off
	v_lshl_add_u64 v[222:223], s[36:37], 0, v[166:167]
	s_mov_b32 m0, s67
	s_nop 0
	global_load_lds_dwordx4 v[222:223], off
	s_waitcnt vmcnt(8)
	s_waitcnt lgkmcnt(0)
	s_barrier
	s_setprio 1
	s_waitcnt lgkmcnt(0)
	v_mfma_scale_f32_16x16x128_f8f6f4 v[114:117], v[10:17], v[206:213], v[114:117], v187, v187 op_sel_hi:[0,0,0]
	v_mfma_scale_f32_16x16x128_f8f6f4 v[126:129], v[2:9], v[206:213], v[126:129], v187, v187 op_sel_hi:[0,0,0]
	v_mfma_scale_f32_16x16x128_f8f6f4 v[158:161], v[2:9], v[190:197], v[158:161], v187, v187 op_sel_hi:[0,0,0]
	v_mfma_scale_f32_16x16x128_f8f6f4 v[154:157], v[10:17], v[190:197], v[154:157], v187, v187 op_sel_hi:[0,0,0]
	v_mfma_scale_f32_16x16x128_f8f6f4 v[118:121], v[10:17], v[198:205], v[118:121], v187, v187 op_sel_hi:[0,0,0]
	v_mfma_scale_f32_16x16x128_f8f6f4 v[122:125], v[2:9], v[198:205], v[122:125], v187, v187 op_sel_hi:[0,0,0]
	v_mfma_scale_f32_16x16x128_f8f6f4 v[110:113], v[2:9], v[214:221], v[110:113], v187, v187 op_sel_hi:[0,0,0]
	v_mfma_scale_f32_16x16x128_f8f6f4 v[106:109], v[10:17], v[214:221], v[106:109], v187, v187 op_sel_hi:[0,0,0]
	s_setprio 0
	s_setprio 1
	v_mfma_scale_f32_16x16x128_f8f6f4 v[102:105], v[18:25], v[214:221], v[102:105], v187, v187 op_sel_hi:[0,0,0]
	v_mfma_scale_f32_16x16x128_f8f6f4 v[98:101], v[26:33], v[214:221], v[98:101], v187, v187 op_sel_hi:[0,0,0]
	v_mfma_scale_f32_16x16x128_f8f6f4 v[146:149], v[26:33], v[190:197], v[146:149], v187, v187 op_sel_hi:[0,0,0]
	v_mfma_scale_f32_16x16x128_f8f6f4 v[150:153], v[18:25], v[190:197], v[150:153], v187, v187 op_sel_hi:[0,0,0]
	v_mfma_scale_f32_16x16x128_f8f6f4 v[142:145], v[18:25], v[198:205], v[142:145], v187, v187 op_sel_hi:[0,0,0]
	v_mfma_scale_f32_16x16x128_f8f6f4 v[138:141], v[26:33], v[198:205], v[138:141], v187, v187 op_sel_hi:[0,0,0]
	v_mfma_scale_f32_16x16x128_f8f6f4 v[130:133], v[26:33], v[206:213], v[130:133], v187, v187 op_sel_hi:[0,0,0]
	v_mfma_scale_f32_16x16x128_f8f6f4 v[134:137], v[18:25], v[206:213], v[134:137], v187, v187 op_sel_hi:[0,0,0]
	s_setprio 0
	s_barrier
	s_add_i32 s36, s72, s43
	v_lshl_add_u64 v[172:173], v[172:173], 0, s[22:23]
	s_mov_b32 m0, s36
	ds_read_b128 v[190:193], v189 offset:49152
	ds_read_b128 v[194:197], v189 offset:50176
	ds_read_b128 v[198:201], v189 offset:51200
	ds_read_b128 v[202:205], v189 offset:52224
	ds_read_b128 v[206:209], v189 offset:53248
	ds_read_b128 v[210:213], v189 offset:54272
	ds_read_b128 v[214:217], v189 offset:55296
	ds_read_b128 v[218:221], v189 offset:56320
	global_load_lds_dwordx4 v[172:173], off
	s_add_i32 m0, s36, 0x2000
	s_add_u32 s8, s8, 0x158080
	v_lshl_add_u64 v[172:173], v[174:175], 0, s[22:23]
	s_addc_u32 s9, s9, 0
	s_add_i32 s36, s73, s43
	global_load_lds_dwordx4 v[172:173], off
	v_lshl_add_u64 v[172:173], s[8:9], 0, v[162:163]
	s_mov_b32 m0, s36
	s_nop 0
	global_load_lds_dwordx4 v[172:173], off
	v_lshl_add_u64 v[172:173], s[8:9], 0, v[166:167]
	s_add_i32 m0, s36, 0x2000
	s_nop 0
	global_load_lds_dwordx4 v[172:173], off
	v_lshl_add_u64 v[172:173], v[176:177], 0, s[22:23]
	s_mov_b32 m0, s69
	s_nop 0
	global_load_lds_dwordx4 v[172:173], off
	v_lshl_add_u64 v[172:173], v[178:179], 0, s[22:23]
	s_mov_b32 m0, s70
	s_nop 0
	global_load_lds_dwordx4 v[172:173], off
	s_waitcnt vmcnt(8)
	s_waitcnt lgkmcnt(0)
	s_barrier
	s_setprio 1
	s_waitcnt lgkmcnt(0)
	v_mfma_scale_f32_16x16x128_f8f6f4 v[62:65], v[2:9], v[206:213], v[62:65], v187, v187 op_sel_hi:[0,0,0]
	v_mfma_scale_f32_16x16x128_f8f6f4 v[58:61], v[10:17], v[206:213], v[58:61], v187, v187 op_sel_hi:[0,0,0]
	v_mfma_scale_f32_16x16x128_f8f6f4 v[90:93], v[10:17], v[190:197], v[90:93], v187, v187 op_sel_hi:[0,0,0]
	v_mfma_scale_f32_16x16x128_f8f6f4 v[94:97], v[2:9], v[190:197], v[94:97], v187, v187 op_sel_hi:[0,0,0]
	v_mfma_scale_f32_16x16x128_f8f6f4 v[78:81], v[2:9], v[198:205], v[78:81], v187, v187 op_sel_hi:[0,0,0]
	v_mfma_scale_f32_16x16x128_f8f6f4 v[74:77], v[10:17], v[198:205], v[74:77], v187, v187 op_sel_hi:[0,0,0]
	v_mfma_scale_f32_16x16x128_f8f6f4 v[42:45], v[10:17], v[214:221], v[42:45], v187, v187 op_sel_hi:[0,0,0]
	v_mfma_scale_f32_16x16x128_f8f6f4 v[46:49], v[2:9], v[214:221], v[46:49], v187, v187 op_sel_hi:[0,0,0]
	s_setprio 0
	s_setprio 1
	v_mfma_scale_f32_16x16x128_f8f6f4 v[38:41], v[18:25], v[214:221], v[38:41], v187, v187 op_sel_hi:[0,0,0]
	v_mfma_scale_f32_16x16x128_f8f6f4 v[34:37], v[26:33], v[214:221], v[34:37], v187, v187 op_sel_hi:[0,0,0]
	v_mfma_scale_f32_16x16x128_f8f6f4 v[82:85], v[26:33], v[190:197], v[82:85], v187, v187 op_sel_hi:[0,0,0]
	v_mfma_scale_f32_16x16x128_f8f6f4 v[86:89], v[18:25], v[190:197], v[86:89], v187, v187 op_sel_hi:[0,0,0]
	v_mfma_scale_f32_16x16x128_f8f6f4 v[70:73], v[18:25], v[198:205], v[70:73], v187, v187 op_sel_hi:[0,0,0]
	v_mfma_scale_f32_16x16x128_f8f6f4 v[66:69], v[26:33], v[198:205], v[66:69], v187, v187 op_sel_hi:[0,0,0]
	v_mfma_scale_f32_16x16x128_f8f6f4 v[50:53], v[26:33], v[206:213], v[50:53], v187, v187 op_sel_hi:[0,0,0]
	v_mfma_scale_f32_16x16x128_f8f6f4 v[54:57], v[18:25], v[206:213], v[54:57], v187, v187 op_sel_hi:[0,0,0]
	s_setprio 0
	s_barrier
	s_add_i32 s71, s71, 2
	s_add_u32 s6, s6, 0x100
	s_addc_u32 s7, s7, 0
	s_cmpk_lt_u32 s71, 0x54
	s_cbranch_scc1 .LBB0_1745
	s_waitcnt vmcnt(0)
	s_cmpk_gt_u32 s40, 0xff
	s_cbranch_scc1 .LBB0_1748
	s_barrier

.LBB0_1807:
	ds_read_b128 v[26:29], v185
	ds_read_b128 v[30:33], v185 offset:1024
	ds_read_b128 v[18:21], v185 offset:2048
	ds_read_b128 v[22:25], v185 offset:3072
	ds_read_b128 v[10:13], v186
	ds_read_b128 v[14:17], v186 offset:1024
	ds_read_b128 v[2:5], v186 offset:2048
	ds_read_b128 v[6:9], v186 offset:3072
	s_add_u32 s28, s26, 0xffea8080
	s_addc_u32 s29, s27, -1
	s_cmpk_eq_i32 s58, 0x52
	s_cselect_b32 s31, s5, s29
	s_cselect_b32 s30, s4, s28
	s_cselect_b32 s29, s25, s57
	s_cselect_b32 s28, s24, s56
	v_lshl_add_u64 v[212:213], s[26:27], 0, v[166:167]
	s_add_i32 m0, s34, 0xc000
	ds_read_b128 v[174:177], v187
	ds_read_b128 v[178:181], v187 offset:1024
	ds_read_b128 v[188:191], v187 offset:2048
	ds_read_b128 v[192:195], v187 offset:3072
	ds_read_b128 v[196:199], v187 offset:4096
	ds_read_b128 v[200:203], v187 offset:5120
	ds_read_b128 v[204:207], v187 offset:6144
	ds_read_b128 v[208:211], v187 offset:7168
	global_load_lds_dwordx4 v[212:213], off
	v_lshl_add_u64 v[212:213], s[26:27], 0, v[168:169]
	s_add_i32 m0, s34, 0xe000
	s_nop 0
	global_load_lds_dwordx4 v[212:213], off
	s_waitcnt vmcnt(8)
	s_waitcnt lgkmcnt(0)
	s_barrier
	s_setprio 1
	s_waitcnt lgkmcnt(0)
	v_mfma_scale_f32_16x16x128_f8f6f4 v[158:161], v[26:33], v[174:181], v[158:161], v1, v1 op_sel_hi:[0,0,0]
	v_mfma_scale_f32_16x16x128_f8f6f4 v[154:157], v[18:25], v[174:181], v[154:157], v1, v1 op_sel_hi:[0,0,0]
	v_mfma_scale_f32_16x16x128_f8f6f4 v[138:141], v[18:25], v[188:195], v[138:141], v1, v1 op_sel_hi:[0,0,0]
	v_mfma_scale_f32_16x16x128_f8f6f4 v[142:145], v[26:33], v[188:195], v[142:145], v1, v1 op_sel_hi:[0,0,0]
	v_mfma_scale_f32_16x16x128_f8f6f4 v[126:129], v[26:33], v[196:203], v[126:129], v1, v1 op_sel_hi:[0,0,0]
	v_mfma_scale_f32_16x16x128_f8f6f4 v[122:125], v[18:25], v[196:203], v[122:125], v1, v1 op_sel_hi:[0,0,0]
	v_mfma_scale_f32_16x16x128_f8f6f4 v[106:109], v[18:25], v[204:211], v[106:109], v1, v1 op_sel_hi:[0,0,0]
	v_mfma_scale_f32_16x16x128_f8f6f4 v[110:113], v[26:33], v[204:211], v[110:113], v1, v1 op_sel_hi:[0,0,0]
	s_setprio 0
	s_setprio 1
	v_mfma_scale_f32_16x16x128_f8f6f4 v[102:105], v[10:17], v[204:211], v[102:105], v1, v1 op_sel_hi:[0,0,0]
	v_mfma_scale_f32_16x16x128_f8f6f4 v[98:101], v[2:9], v[204:211], v[98:101], v1, v1 op_sel_hi:[0,0,0]
	v_mfma_scale_f32_16x16x128_f8f6f4 v[146:149], v[2:9], v[174:181], v[146:149], v1, v1 op_sel_hi:[0,0,0]
	v_mfma_scale_f32_16x16x128_f8f6f4 v[150:153], v[10:17], v[174:181], v[150:153], v1, v1 op_sel_hi:[0,0,0]
	v_mfma_scale_f32_16x16x128_f8f6f4 v[134:137], v[10:17], v[188:195], v[134:137], v1, v1 op_sel_hi:[0,0,0]
	v_mfma_scale_f32_16x16x128_f8f6f4 v[130:133], v[2:9], v[188:195], v[130:133], v1, v1 op_sel_hi:[0,0,0]
	v_mfma_scale_f32_16x16x128_f8f6f4 v[114:117], v[2:9], v[196:203], v[114:117], v1, v1 op_sel_hi:[0,0,0]
	v_mfma_scale_f32_16x16x128_f8f6f4 v[118:121], v[10:17], v[196:203], v[118:121], v1, v1 op_sel_hi:[0,0,0]
	s_setprio 0
	s_barrier
	s_add_i32 s59, s42, s3
	v_lshl_add_u64 v[174:175], s[28:29], 0, v[164:165]
	s_mov_b32 m0, s59
	ds_read_b128 v[188:191], v187 offset:16384
	ds_read_b128 v[192:195], v187 offset:17408
	ds_read_b128 v[196:199], v187 offset:18432
	ds_read_b128 v[200:203], v187 offset:19456
	ds_read_b128 v[204:207], v187 offset:20480
	ds_read_b128 v[208:211], v187 offset:21504
	ds_read_b128 v[212:215], v187 offset:22528
	ds_read_b128 v[216:219], v187 offset:23552
	global_load_lds_dwordx4 v[174:175], off
	s_add_i32 m0, s59, 0x2000
	s_add_u32 s60, s28, 0x158000
	v_lshl_add_u64 v[176:177], s[28:29], 0, v[162:163]
	s_addc_u32 s61, s29, 0
	s_add_i32 s59, s43, s3
	global_load_lds_dwordx4 v[176:177], off
	v_lshl_add_u64 v[178:179], s[60:61], 0, v[164:165]
	s_mov_b32 m0, s59
	v_lshl_add_u64 v[180:181], s[30:31], 0, v[162:163]
	global_load_lds_dwordx4 v[178:179], off
	v_lshl_add_u64 v[178:179], s[60:61], 0, v[162:163]
	s_add_i32 m0, s59, 0x2000
	s_nop 0
	global_load_lds_dwordx4 v[178:179], off
	v_lshl_add_u64 v[178:179], s[30:31], 0, v[164:165]
	s_mov_b32 m0, s34
	s_nop 0
	global_load_lds_dwordx4 v[178:179], off
	s_mov_b32 m0, s35
	s_nop 0
	global_load_lds_dwordx4 v[180:181], off
	s_waitcnt vmcnt(8)
	s_waitcnt lgkmcnt(0)
	s_barrier
	s_setprio 1
	s_waitcnt lgkmcnt(0)
	v_mfma_scale_f32_16x16x128_f8f6f4 v[78:81], v[26:33], v[196:203], v[78:81], v1, v1 op_sel_hi:[0,0,0]
	v_mfma_scale_f32_16x16x128_f8f6f4 v[74:77], v[18:25], v[196:203], v[74:77], v1, v1 op_sel_hi:[0,0,0]
	v_mfma_scale_f32_16x16x128_f8f6f4 v[90:93], v[18:25], v[188:195], v[90:93], v1, v1 op_sel_hi:[0,0,0]
	v_mfma_scale_f32_16x16x128_f8f6f4 v[94:97], v[26:33], v[188:195], v[94:97], v1, v1 op_sel_hi:[0,0,0]
	v_mfma_scale_f32_16x16x128_f8f6f4 v[62:65], v[26:33], v[204:211], v[62:65], v1, v1 op_sel_hi:[0,0,0]
	v_mfma_scale_f32_16x16x128_f8f6f4 v[58:61], v[18:25], v[204:211], v[58:61], v1, v1 op_sel_hi:[0,0,0]
	v_mfma_scale_f32_16x16x128_f8f6f4 v[42:45], v[18:25], v[212:219], v[42:45], v1, v1 op_sel_hi:[0,0,0]
	v_mfma_scale_f32_16x16x128_f8f6f4 v[54:57], v[26:33], v[212:219], v[54:57], v1, v1 op_sel_hi:[0,0,0]
	s_setprio 0
	s_setprio 1
	v_mfma_scale_f32_16x16x128_f8f6f4 v[38:41], v[10:17], v[212:219], v[38:41], v1, v1 op_sel_hi:[0,0,0]
	v_mfma_scale_f32_16x16x128_f8f6f4 v[34:37], v[2:9], v[212:219], v[34:37], v1, v1 op_sel_hi:[0,0,0]
	v_mfma_scale_f32_16x16x128_f8f6f4 v[82:85], v[2:9], v[188:195], v[82:85], v1, v1 op_sel_hi:[0,0,0]
	v_mfma_scale_f32_16x16x128_f8f6f4 v[86:89], v[10:17], v[188:195], v[86:89], v1, v1 op_sel_hi:[0,0,0]
	v_mfma_scale_f32_16x16x128_f8f6f4 v[70:73], v[10:17], v[196:203], v[70:73], v1, v1 op_sel_hi:[0,0,0]
	v_mfma_scale_f32_16x16x128_f8f6f4 v[66:69], v[2:9], v[196:203], v[66:69], v1, v1 op_sel_hi:[0,0,0]
	v_mfma_scale_f32_16x16x128_f8f6f4 v[46:49], v[2:9], v[204:211], v[46:49], v1, v1 op_sel_hi:[0,0,0]
	v_mfma_scale_f32_16x16x128_f8f6f4 v[50:53], v[10:17], v[204:211], v[50:53], v1, v1 op_sel_hi:[0,0,0]
	s_setprio 0
	s_barrier
	s_add_i32 s59, 0, 0x18000
	s_add_i32 s60, 0, 0x1c000
	v_add_u32_e32 v14, s59, v183
	v_add_u32_e32 v30, s60, v183
	ds_read_b128 v[2:5], v14
	ds_read_b128 v[6:9], v14 offset:1024
	ds_read_b128 v[10:13], v14 offset:2048
	ds_read_b128 v[14:17], v14 offset:3072
	ds_read_b128 v[18:21], v30
	ds_read_b128 v[22:25], v30 offset:1024
	ds_read_b128 v[26:29], v30 offset:2048
	ds_read_b128 v[30:33], v30 offset:3072
	s_add_u32 s30, s30, 0x158000
	s_addc_u32 s31, s31, 0
	s_mov_b32 m0, s36
	v_lshl_add_u64 v[220:221], s[30:31], 0, v[164:165]
	ds_read_b128 v[188:191], v187 offset:32768
	ds_read_b128 v[192:195], v187 offset:33792
	ds_read_b128 v[196:199], v187 offset:34816
	ds_read_b128 v[200:203], v187 offset:35840
	ds_read_b128 v[204:207], v187 offset:36864
	ds_read_b128 v[208:211], v187 offset:37888
	ds_read_b128 v[212:215], v187 offset:38912
	ds_read_b128 v[216:219], v187 offset:39936
	global_load_lds_dwordx4 v[220:221], off
	v_lshl_add_u64 v[220:221], s[30:31], 0, v[162:163]
	s_mov_b32 m0, s37
	s_nop 0
	global_load_lds_dwordx4 v[220:221], off
	s_waitcnt vmcnt(8)
	s_waitcnt lgkmcnt(0)
	s_barrier
	s_setprio 1
	s_waitcnt lgkmcnt(0)
	v_mfma_scale_f32_16x16x128_f8f6f4 v[122:125], v[10:17], v[204:211], v[122:125], v1, v1 op_sel_hi:[0,0,0]
	v_mfma_scale_f32_16x16x128_f8f6f4 v[126:129], v[2:9], v[204:211], v[126:129], v1, v1 op_sel_hi:[0,0,0]
	v_mfma_scale_f32_16x16x128_f8f6f4 v[158:161], v[2:9], v[188:195], v[158:161], v1, v1 op_sel_hi:[0,0,0]
	v_mfma_scale_f32_16x16x128_f8f6f4 v[154:157], v[10:17], v[188:195], v[154:157], v1, v1 op_sel_hi:[0,0,0]
	v_mfma_scale_f32_16x16x128_f8f6f4 v[138:141], v[10:17], v[196:203], v[138:141], v1, v1 op_sel_hi:[0,0,0]
	v_mfma_scale_f32_16x16x128_f8f6f4 v[142:145], v[2:9], v[196:203], v[142:145], v1, v1 op_sel_hi:[0,0,0]
	v_mfma_scale_f32_16x16x128_f8f6f4 v[110:113], v[2:9], v[212:219], v[110:113], v1, v1 op_sel_hi:[0,0,0]
	v_mfma_scale_f32_16x16x128_f8f6f4 v[106:109], v[10:17], v[212:219], v[106:109], v1, v1 op_sel_hi:[0,0,0]
	s_setprio 0
	s_setprio 1
	v_mfma_scale_f32_16x16x128_f8f6f4 v[102:105], v[18:25], v[212:219], v[102:105], v1, v1 op_sel_hi:[0,0,0]
	v_mfma_scale_f32_16x16x128_f8f6f4 v[98:101], v[26:33], v[212:219], v[98:101], v1, v1 op_sel_hi:[0,0,0]
	v_mfma_scale_f32_16x16x128_f8f6f4 v[146:149], v[26:33], v[188:195], v[146:149], v1, v1 op_sel_hi:[0,0,0]
	v_mfma_scale_f32_16x16x128_f8f6f4 v[150:153], v[18:25], v[188:195], v[150:153], v1, v1 op_sel_hi:[0,0,0]
	v_mfma_scale_f32_16x16x128_f8f6f4 v[134:137], v[18:25], v[196:203], v[134:137], v1, v1 op_sel_hi:[0,0,0]
	v_mfma_scale_f32_16x16x128_f8f6f4 v[130:133], v[26:33], v[196:203], v[130:133], v1, v1 op_sel_hi:[0,0,0]
	v_mfma_scale_f32_16x16x128_f8f6f4 v[114:117], v[26:33], v[204:211], v[114:117], v1, v1 op_sel_hi:[0,0,0]
	v_mfma_scale_f32_16x16x128_f8f6f4 v[118:121], v[18:25], v[204:211], v[118:121], v1, v1 op_sel_hi:[0,0,0]
	s_setprio 0
	s_barrier
	s_add_i32 s30, s59, s3
	v_lshl_add_u64 v[174:175], v[174:175], 0, s[10:11]
	s_mov_b32 m0, s30
	ds_read_b128 v[188:191], v187 offset:49152
	ds_read_b128 v[192:195], v187 offset:50176
	ds_read_b128 v[196:199], v187 offset:51200
	ds_read_b128 v[200:203], v187 offset:52224
	ds_read_b128 v[204:207], v187 offset:53248
	ds_read_b128 v[208:211], v187 offset:54272
	ds_read_b128 v[212:215], v187 offset:55296
	ds_read_b128 v[216:219], v187 offset:56320
	global_load_lds_dwordx4 v[174:175], off
	s_add_i32 m0, s30, 0x2000
	s_add_u32 s28, s28, 0x158080
	v_lshl_add_u64 v[174:175], v[176:177], 0, s[10:11]
	s_addc_u32 s29, s29, 0
	s_add_i32 s30, s60, s3
	global_load_lds_dwordx4 v[174:175], off
	v_lshl_add_u64 v[174:175], s[28:29], 0, v[164:165]
	s_mov_b32 m0, s30
	s_nop 0
	global_load_lds_dwordx4 v[174:175], off
	v_lshl_add_u64 v[174:175], s[28:29], 0, v[162:163]
	s_add_i32 m0, s30, 0x2000
	s_nop 0
	global_load_lds_dwordx4 v[174:175], off
	v_lshl_add_u64 v[174:175], v[178:179], 0, s[10:11]
	s_mov_b32 m0, s40
	s_nop 0
	global_load_lds_dwordx4 v[174:175], off
	v_lshl_add_u64 v[174:175], v[180:181], 0, s[10:11]
	s_mov_b32 m0, s41
	s_nop 0
	global_load_lds_dwordx4 v[174:175], off
	s_waitcnt vmcnt(8)
	s_waitcnt lgkmcnt(0)
	s_barrier
	s_setprio 1
	s_waitcnt lgkmcnt(0)
	v_mfma_scale_f32_16x16x128_f8f6f4 v[62:65], v[2:9], v[204:211], v[62:65], v1, v1 op_sel_hi:[0,0,0]
	v_mfma_scale_f32_16x16x128_f8f6f4 v[58:61], v[10:17], v[204:211], v[58:61], v1, v1 op_sel_hi:[0,0,0]
	v_mfma_scale_f32_16x16x128_f8f6f4 v[90:93], v[10:17], v[188:195], v[90:93], v1, v1 op_sel_hi:[0,0,0]
	v_mfma_scale_f32_16x16x128_f8f6f4 v[94:97], v[2:9], v[188:195], v[94:97], v1, v1 op_sel_hi:[0,0,0]
	v_mfma_scale_f32_16x16x128_f8f6f4 v[78:81], v[2:9], v[196:203], v[78:81], v1, v1 op_sel_hi:[0,0,0]
	v_mfma_scale_f32_16x16x128_f8f6f4 v[74:77], v[10:17], v[196:203], v[74:77], v1, v1 op_sel_hi:[0,0,0]
	v_mfma_scale_f32_16x16x128_f8f6f4 v[42:45], v[10:17], v[212:219], v[42:45], v1, v1 op_sel_hi:[0,0,0]
	v_mfma_scale_f32_16x16x128_f8f6f4 v[54:57], v[2:9], v[212:219], v[54:57], v1, v1 op_sel_hi:[0,0,0]
	s_setprio 0
	s_setprio 1
	v_mfma_scale_f32_16x16x128_f8f6f4 v[38:41], v[18:25], v[212:219], v[38:41], v1, v1 op_sel_hi:[0,0,0]
	v_mfma_scale_f32_16x16x128_f8f6f4 v[34:37], v[26:33], v[212:219], v[34:37], v1, v1 op_sel_hi:[0,0,0]
	v_mfma_scale_f32_16x16x128_f8f6f4 v[82:85], v[26:33], v[188:195], v[82:85], v1, v1 op_sel_hi:[0,0,0]
	v_mfma_scale_f32_16x16x128_f8f6f4 v[86:89], v[18:25], v[188:195], v[86:89], v1, v1 op_sel_hi:[0,0,0]
	v_mfma_scale_f32_16x16x128_f8f6f4 v[70:73], v[18:25], v[196:203], v[70:73], v1, v1 op_sel_hi:[0,0,0]
	v_mfma_scale_f32_16x16x128_f8f6f4 v[66:69], v[26:33], v[196:203], v[66:69], v1, v1 op_sel_hi:[0,0,0]
	v_mfma_scale_f32_16x16x128_f8f6f4 v[46:49], v[26:33], v[204:211], v[46:49], v1, v1 op_sel_hi:[0,0,0]
	v_mfma_scale_f32_16x16x128_f8f6f4 v[50:53], v[18:25], v[204:211], v[50:53], v1, v1 op_sel_hi:[0,0,0]
	s_setprio 0
	s_barrier
	s_add_i32 s58, s58, 2
	s_add_u32 s26, s26, 0x100
	s_addc_u32 s27, s27, 0
	s_add_u32 s56, s56, 0x100
	s_addc_u32 s57, s57, 0
	s_cmpk_gt_u32 s58, 0x53
	s_cbranch_scc0 .LBB0_1807
	s_and_b64 vcc, exec, s[12:13]
	s_cbranch_vccz .LBB0_1810
	s_barrier
